# EpiIn sigmoid-gate (u8) and silu (fp8) branches rewritten by hand: in-place staged exp/rcp, packed-f32 scale/add/fma with SGPR/inline broadcast constants (708+770 vs 1000+1064 instr), on top of rotary
# speedup vs baseline: 1.0155x; 1.0009x over previous
; #define GAS __attribute__((address_space(1)))
;     DI void operator()(const f32x4 (&acc)[2][2][4][2], const Unit& u, int wr, int wc, int fr, int fq) const {
;     ...
;         if (pn >= 12 && pn < 24) {
;             bf16_t* base = pn < 18 ? qd : kd; const int tq = pn < 18 ? pn - 12 : pn - 18; const float sc = pn < 18 ? 0.125f * LOG2E * W8_INV : W8_INV;
;             float fre[8];
; #pragma unroll
;             for (int i = 0; i < 8; ++i) fre[i] = __builtin_amdgcn_exp2f(-(float)(8 * fq + i) * (13.287712379549449f / 32.0f)) * 0.15915494309189535f;
;             int posv[8];
; #pragma unroll
;             for (int q = 0; q < 8; ++q) posv[q] = ((const GAS int*)pos)[row0 + (q >> 2) * 128 + (q & 3) * 16];
; #pragma unroll
;             for (int ai = 0; ai < 2; ++ai) {
; #pragma unroll
;                 for (int m = 0; m < 4; ++m) {
;                     const int r = row0 + ai * 128 + m * 16; const float p = (float)posv[ai * 4 + m];
;                     unsigned char* rowp = (unsigned char*)base + dil_row(4 * tq + wc, r) + 8 * fq;
;                     u32x2 w1, w2;
; #pragma unroll
;                     for (int n = 0; n < 2; ++n) { f32x4 o1, o2;
; #pragma unroll
;                         for (int j = 0; j < 4; ++j) {
;                             float a = p * fre[n * 4 + j]; a = a - __builtin_floorf(a);
;                             const float sn = __builtin_amdgcn_sinf(a), cs = __builtin_amdgcn_cosf(a);
;                             const float x1 = acc[ai][0][m][n][j], x2 = acc[ai][1][m][n][j];
;                             o1[j] = (x1 * cs - x2 * sn) * sc; o2[j] = (x2 * cs + x1 * sn) * sc;
;                         }
;     ...
;                     for (int m = 0; m < 4; ++m) { unsigned char* rowp = (unsigned char*)gt + (size_t)(row0 + ai * 128 + m * 16) * 2048 + (pn - 30) * 256 + wc * 32 + 8 * fq;
;                         u32x2 o[2];
; #pragma unroll
;                         for (int bj = 0; bj < 2; ++bj) {
; #pragma unroll
;                             for (int n = 0; n < 2; ++n) { const f32x4 v = acc[ai][bj][m][n];
;                                 o[bj][n] = (unsigned)(sigmoid64_(v[0]) * 255.0f + 0.5f) | ((unsigned)(sigmoid64_(v[1]) * 255.0f + 0.5f) << 8) | ((unsigned)(sigmoid64_(v[2]) * 255.0f + 0.5f) << 16) | ((unsigned)(sigmoid64_(v[3]) * 255.0f + 0.5f) << 24); } }
;                         st_pair16(rowp, 128, o[0], o[1], fq); }
.LBB0_283:
	s_lshl_b32 s4, s16, 8
	s_add_i32 s4, s4, s87
	v_add_u32_e32 v10, s4, v6
	s_add_i32 s4, s43, -12
	s_cmp_gt_u32 s4, 11
	s_mov_b64 s[16:17], -1
	s_cbranch_scc0 .LBB0_299
	s_cmp_lg_u32 s43, 38
	s_cbranch_scc0 .LBB0_310
	s_cmp_gt_i32 s43, 1
	s_cbranch_scc0 .LBB0_301
	s_cmp_gt_u32 s43, 3
	s_cbranch_scc0 .LBB0_302
	s_cmp_gt_u32 s43, 7
	s_cbranch_scc0 .LBB0_297
	s_cmp_gt_u32 s43, 11
	s_cbranch_scc0 .LBB0_294
	s_cmp_lt_u32 s43, 30
	s_cbranch_scc1 .LBB0_291
	s_lshl_b32 s4, s43, 8
	s_addk_i32 s4, 0xe200
	s_ashr_i32 s5, s4, 31
	v_bfe_i32 v6, v18, 0, 1
	v_and_b32_e32 v14, 0x78, v6
	v_mov_b32_e32 v15, v4
	v_ashrrev_i32_e32 v11, 31, v10
	v_lshlrev_b64 v[6:7], 11, v[10:11]
	v_readlane_b32 s6, v255, 24
	v_readlane_b32 s7, v255, 25
	v_lshl_add_u64 v[6:7], s[6:7], 0, v[6:7]
	v_lshl_add_u64 v[6:7], v[6:7], 0, s[4:5]
	v_readlane_b32 s4, v255, 36
	v_readlane_b32 s5, v255, 37
	v_lshl_add_u64 v[16:17], v[6:7], 0, s[4:5]
	v_lshlrev_b32_e32 v12, 3, v18
	v_ashrrev_i32_e32 v13, 31, v12
	v_lshl_add_u64 v[12:13], v[16:17], 0, v[12:13]
	v_lshl_add_u64 v[12:13], v[12:13], 0, v[14:15]
	s_mov_b32 s6, 0x437f0000
	s_mov_b32 s4, 0xbcb8aa3b
	s_mov_b64 s[16:17], 0
	v_pk_mul_f32 v[150:151], v[150:151], s[4:5] op_sel_hi:[1,0]
	v_pk_mul_f32 v[152:153], v[152:153], s[4:5] op_sel_hi:[1,0]
	v_pk_mul_f32 v[154:155], v[154:155], s[4:5] op_sel_hi:[1,0]
	v_pk_mul_f32 v[156:157], v[156:157], s[4:5] op_sel_hi:[1,0]
	v_pk_mul_f32 v[158:159], v[158:159], s[4:5] op_sel_hi:[1,0]
	v_pk_mul_f32 v[160:161], v[160:161], s[4:5] op_sel_hi:[1,0]
	v_pk_mul_f32 v[162:163], v[162:163], s[4:5] op_sel_hi:[1,0]
	v_pk_mul_f32 v[164:165], v[164:165], s[4:5] op_sel_hi:[1,0]
	v_exp_f32_e32 v150, v150
	v_exp_f32_e32 v151, v151
	v_exp_f32_e32 v152, v152
	v_exp_f32_e32 v153, v153
	v_exp_f32_e32 v154, v154
	v_exp_f32_e32 v155, v155
	v_exp_f32_e32 v156, v156
	v_exp_f32_e32 v157, v157
	v_exp_f32_e32 v158, v158
	v_exp_f32_e32 v159, v159
	v_exp_f32_e32 v160, v160
	v_exp_f32_e32 v161, v161
	v_exp_f32_e32 v162, v162
	v_exp_f32_e32 v163, v163
	v_exp_f32_e32 v164, v164
	v_exp_f32_e32 v165, v165
	v_pk_add_f32 v[150:151], v[150:151], 1.0 op_sel_hi:[1,0]
	v_pk_add_f32 v[152:153], v[152:153], 1.0 op_sel_hi:[1,0]
	v_pk_add_f32 v[154:155], v[154:155], 1.0 op_sel_hi:[1,0]
	v_pk_add_f32 v[156:157], v[156:157], 1.0 op_sel_hi:[1,0]
	v_pk_add_f32 v[158:159], v[158:159], 1.0 op_sel_hi:[1,0]
	v_pk_add_f32 v[160:161], v[160:161], 1.0 op_sel_hi:[1,0]
	v_pk_add_f32 v[162:163], v[162:163], 1.0 op_sel_hi:[1,0]
	v_pk_add_f32 v[164:165], v[164:165], 1.0 op_sel_hi:[1,0]
	v_rcp_f32_e32 v150, v150
	v_rcp_f32_e32 v151, v151
	v_rcp_f32_e32 v152, v152
	v_rcp_f32_e32 v153, v153
	v_rcp_f32_e32 v154, v154
	v_rcp_f32_e32 v155, v155
	v_rcp_f32_e32 v156, v156
	v_rcp_f32_e32 v157, v157
	v_rcp_f32_e32 v158, v158
	v_rcp_f32_e32 v159, v159
	v_rcp_f32_e32 v160, v160
	v_rcp_f32_e32 v161, v161
	v_rcp_f32_e32 v162, v162
	v_rcp_f32_e32 v163, v163
	v_rcp_f32_e32 v164, v164
	v_rcp_f32_e32 v165, v165
	v_pk_fma_f32 v[150:151], v[150:151], s[6:7], 0.5 op_sel_hi:[1,0,0]
	v_pk_fma_f32 v[152:153], v[152:153], s[6:7], 0.5 op_sel_hi:[1,0,0]
	v_pk_fma_f32 v[154:155], v[154:155], s[6:7], 0.5 op_sel_hi:[1,0,0]
	v_pk_fma_f32 v[156:157], v[156:157], s[6:7], 0.5 op_sel_hi:[1,0,0]
	v_pk_fma_f32 v[158:159], v[158:159], s[6:7], 0.5 op_sel_hi:[1,0,0]
	v_pk_fma_f32 v[160:161], v[160:161], s[6:7], 0.5 op_sel_hi:[1,0,0]
	v_pk_fma_f32 v[162:163], v[162:163], s[6:7], 0.5 op_sel_hi:[1,0,0]
	v_pk_fma_f32 v[164:165], v[164:165], s[6:7], 0.5 op_sel_hi:[1,0,0]
	v_cvt_u32_f32_e32 v158, v158
	v_cvt_u32_f32_e32 v159, v159
	v_cvt_u32_f32_sdwa v160, v160 dst_sel:WORD_1 dst_unused:UNUSED_PAD src0_sel:DWORD
	v_cvt_u32_f32_sdwa v161, v161 dst_sel:BYTE_3 dst_unused:UNUSED_PAD src0_sel:DWORD
	v_cvt_u32_f32_e32 v150, v150
	v_cvt_u32_f32_e32 v151, v151
	v_cvt_u32_f32_sdwa v152, v152 dst_sel:WORD_1 dst_unused:UNUSED_PAD src0_sel:DWORD
	v_cvt_u32_f32_sdwa v153, v153 dst_sel:BYTE_3 dst_unused:UNUSED_PAD src0_sel:DWORD
	v_cvt_u32_f32_e32 v162, v162
	v_cvt_u32_f32_e32 v163, v163
	v_cvt_u32_f32_sdwa v164, v164 dst_sel:WORD_1 dst_unused:UNUSED_PAD src0_sel:DWORD
	v_cvt_u32_f32_sdwa v165, v165 dst_sel:BYTE_3 dst_unused:UNUSED_PAD src0_sel:DWORD
	v_cvt_u32_f32_e32 v154, v154
	v_cvt_u32_f32_e32 v155, v155
	v_cvt_u32_f32_sdwa v156, v156 dst_sel:WORD_1 dst_unused:UNUSED_PAD src0_sel:DWORD
	v_cvt_u32_f32_sdwa v157, v157 dst_sel:BYTE_3 dst_unused:UNUSED_PAD src0_sel:DWORD
	v_lshl_or_b32 v158, v159, 8, v158
	v_lshl_or_b32 v150, v151, 8, v150
	v_lshl_or_b32 v162, v163, 8, v162
	v_lshl_or_b32 v154, v155, 8, v154
	v_or3_b32 v158, v158, v160, v161
	v_or3_b32 v159, v150, v152, v153
	v_or3_b32 v160, v162, v164, v165
	v_or3_b32 v161, v154, v156, v157
	s_nop 1
	v_permlane16_swap_b32_e32 v158, v160
	v_permlane16_swap_b32_e32 v159, v161
	global_store_dwordx4 v[12:13], v[158:161], off
	v_pk_mul_f32 v[134:135], v[134:135], s[4:5] op_sel_hi:[1,0]
	v_pk_mul_f32 v[136:137], v[136:137], s[4:5] op_sel_hi:[1,0]
	v_pk_mul_f32 v[138:139], v[138:139], s[4:5] op_sel_hi:[1,0]
	v_pk_mul_f32 v[140:141], v[140:141], s[4:5] op_sel_hi:[1,0]
	v_pk_mul_f32 v[142:143], v[142:143], s[4:5] op_sel_hi:[1,0]
	v_pk_mul_f32 v[144:145], v[144:145], s[4:5] op_sel_hi:[1,0]
	v_pk_mul_f32 v[146:147], v[146:147], s[4:5] op_sel_hi:[1,0]
	v_pk_mul_f32 v[148:149], v[148:149], s[4:5] op_sel_hi:[1,0]
	v_exp_f32_e32 v134, v134
	v_exp_f32_e32 v135, v135
	v_exp_f32_e32 v136, v136
	v_exp_f32_e32 v137, v137
	v_exp_f32_e32 v138, v138
	v_exp_f32_e32 v139, v139
	v_exp_f32_e32 v140, v140
	v_exp_f32_e32 v141, v141
	v_exp_f32_e32 v142, v142
	v_exp_f32_e32 v143, v143
	v_exp_f32_e32 v144, v144
	v_exp_f32_e32 v145, v145
	v_exp_f32_e32 v146, v146
	v_exp_f32_e32 v147, v147
; DI float sigmoid64_(float x64) { return __builtin_amdgcn_rcpf(1.0f + __builtin_amdgcn_exp2f(x64 * (-LOG2E * W8_INV))); }
;     DI void operator()(const f32x4 (&acc)[2][2][4][2], const Unit& u, int wr, int wc, int fr, int fq) const {
;     ...
;                     for (int m = 0; m < 4; ++m) { unsigned char* rowp = (unsigned char*)gt + (size_t)(row0 + ai * 128 + m * 16) * 2048 + (pn - 30) * 256 + wc * 32 + 8 * fq;
;                         u32x2 o[2];
; #pragma unroll
;                         for (int bj = 0; bj < 2; ++bj) {
; #pragma unroll
;                             for (int n = 0; n < 2; ++n) { const f32x4 v = acc[ai][bj][m][n];
;                                 o[bj][n] = (unsigned)(sigmoid64_(v[0]) * 255.0f + 0.5f) | ((unsigned)(sigmoid64_(v[1]) * 255.0f + 0.5f) << 8) | ((unsigned)(sigmoid64_(v[2]) * 255.0f + 0.5f) << 16) | ((unsigned)(sigmoid64_(v[3]) * 255.0f + 0.5f) << 24); } }
;                         st_pair16(rowp, 128, o[0], o[1], fq); }
	v_exp_f32_e32 v148, v148
	v_exp_f32_e32 v149, v149
	v_pk_add_f32 v[134:135], v[134:135], 1.0 op_sel_hi:[1,0]
	v_pk_add_f32 v[136:137], v[136:137], 1.0 op_sel_hi:[1,0]
	v_pk_add_f32 v[138:139], v[138:139], 1.0 op_sel_hi:[1,0]
	v_pk_add_f32 v[140:141], v[140:141], 1.0 op_sel_hi:[1,0]
	v_pk_add_f32 v[142:143], v[142:143], 1.0 op_sel_hi:[1,0]
	v_pk_add_f32 v[144:145], v[144:145], 1.0 op_sel_hi:[1,0]
	v_pk_add_f32 v[146:147], v[146:147], 1.0 op_sel_hi:[1,0]
	v_pk_add_f32 v[148:149], v[148:149], 1.0 op_sel_hi:[1,0]
	v_rcp_f32_e32 v134, v134
	v_rcp_f32_e32 v135, v135
	v_rcp_f32_e32 v136, v136
	v_rcp_f32_e32 v137, v137
	v_rcp_f32_e32 v138, v138
	v_rcp_f32_e32 v139, v139
	v_rcp_f32_e32 v140, v140
	v_rcp_f32_e32 v141, v141
	v_rcp_f32_e32 v142, v142
	v_rcp_f32_e32 v143, v143
	v_rcp_f32_e32 v144, v144
	v_rcp_f32_e32 v145, v145
	v_rcp_f32_e32 v146, v146
	v_rcp_f32_e32 v147, v147
	v_rcp_f32_e32 v148, v148
	v_rcp_f32_e32 v149, v149
	v_pk_fma_f32 v[134:135], v[134:135], s[6:7], 0.5 op_sel_hi:[1,0,0]
	v_pk_fma_f32 v[136:137], v[136:137], s[6:7], 0.5 op_sel_hi:[1,0,0]
	v_pk_fma_f32 v[138:139], v[138:139], s[6:7], 0.5 op_sel_hi:[1,0,0]
	v_pk_fma_f32 v[140:141], v[140:141], s[6:7], 0.5 op_sel_hi:[1,0,0]
	v_pk_fma_f32 v[142:143], v[142:143], s[6:7], 0.5 op_sel_hi:[1,0,0]
	v_pk_fma_f32 v[144:145], v[144:145], s[6:7], 0.5 op_sel_hi:[1,0,0]
	v_pk_fma_f32 v[146:147], v[146:147], s[6:7], 0.5 op_sel_hi:[1,0,0]
	v_pk_fma_f32 v[148:149], v[148:149], s[6:7], 0.5 op_sel_hi:[1,0,0]
	v_cvt_u32_f32_e32 v142, v142
	v_cvt_u32_f32_e32 v143, v143
	v_cvt_u32_f32_sdwa v144, v144 dst_sel:WORD_1 dst_unused:UNUSED_PAD src0_sel:DWORD
	v_cvt_u32_f32_sdwa v145, v145 dst_sel:BYTE_3 dst_unused:UNUSED_PAD src0_sel:DWORD
	v_cvt_u32_f32_e32 v134, v134
	v_cvt_u32_f32_e32 v135, v135
	v_cvt_u32_f32_sdwa v136, v136 dst_sel:WORD_1 dst_unused:UNUSED_PAD src0_sel:DWORD
	v_cvt_u32_f32_sdwa v137, v137 dst_sel:BYTE_3 dst_unused:UNUSED_PAD src0_sel:DWORD
	v_cvt_u32_f32_e32 v146, v146
	v_cvt_u32_f32_e32 v147, v147
	v_cvt_u32_f32_sdwa v148, v148 dst_sel:WORD_1 dst_unused:UNUSED_PAD src0_sel:DWORD
	v_cvt_u32_f32_sdwa v149, v149 dst_sel:BYTE_3 dst_unused:UNUSED_PAD src0_sel:DWORD
	v_cvt_u32_f32_e32 v138, v138
	v_cvt_u32_f32_e32 v139, v139
	v_cvt_u32_f32_sdwa v140, v140 dst_sel:WORD_1 dst_unused:UNUSED_PAD src0_sel:DWORD
	v_cvt_u32_f32_sdwa v141, v141 dst_sel:BYTE_3 dst_unused:UNUSED_PAD src0_sel:DWORD
	v_lshl_or_b32 v142, v143, 8, v142
	v_lshl_or_b32 v134, v135, 8, v134
	v_lshl_or_b32 v146, v147, 8, v146
	v_lshl_or_b32 v138, v139, 8, v138
	v_or3_b32 v142, v142, v144, v145
	v_or3_b32 v143, v134, v136, v137
	v_or3_b32 v144, v146, v148, v149
	v_or3_b32 v145, v138, v140, v141
	v_add_co_u32_e32 v14, vcc, 0x8000, v12
	s_nop 0
	v_permlane16_swap_b32_e32 v142, v144
	v_addc_co_u32_e32 v15, vcc, 0, v13, vcc
	v_permlane16_swap_b32_e32 v143, v145
	global_store_dwordx4 v[14:15], v[142:145], off
	v_pk_mul_f32 v[118:119], v[118:119], s[4:5] op_sel_hi:[1,0]
	v_pk_mul_f32 v[120:121], v[120:121], s[4:5] op_sel_hi:[1,0]
	v_pk_mul_f32 v[122:123], v[122:123], s[4:5] op_sel_hi:[1,0]
	v_pk_mul_f32 v[124:125], v[124:125], s[4:5] op_sel_hi:[1,0]
	v_pk_mul_f32 v[126:127], v[126:127], s[4:5] op_sel_hi:[1,0]
	v_pk_mul_f32 v[128:129], v[128:129], s[4:5] op_sel_hi:[1,0]
	v_pk_mul_f32 v[130:131], v[130:131], s[4:5] op_sel_hi:[1,0]
	v_pk_mul_f32 v[132:133], v[132:133], s[4:5] op_sel_hi:[1,0]
	v_exp_f32_e32 v118, v118
	v_exp_f32_e32 v119, v119
	v_exp_f32_e32 v120, v120
	v_exp_f32_e32 v121, v121
	v_exp_f32_e32 v122, v122
	v_exp_f32_e32 v123, v123
	v_exp_f32_e32 v124, v124
	v_exp_f32_e32 v125, v125
	v_exp_f32_e32 v126, v126
	v_exp_f32_e32 v127, v127
	v_exp_f32_e32 v128, v128
	v_exp_f32_e32 v129, v129
	v_exp_f32_e32 v130, v130
	v_exp_f32_e32 v131, v131
	v_exp_f32_e32 v132, v132
	v_exp_f32_e32 v133, v133
	v_pk_add_f32 v[118:119], v[118:119], 1.0 op_sel_hi:[1,0]
	v_pk_add_f32 v[120:121], v[120:121], 1.0 op_sel_hi:[1,0]
	v_pk_add_f32 v[122:123], v[122:123], 1.0 op_sel_hi:[1,0]
	v_pk_add_f32 v[124:125], v[124:125], 1.0 op_sel_hi:[1,0]
	v_pk_add_f32 v[126:127], v[126:127], 1.0 op_sel_hi:[1,0]
	v_pk_add_f32 v[128:129], v[128:129], 1.0 op_sel_hi:[1,0]
	v_pk_add_f32 v[130:131], v[130:131], 1.0 op_sel_hi:[1,0]
	v_pk_add_f32 v[132:133], v[132:133], 1.0 op_sel_hi:[1,0]
	v_rcp_f32_e32 v118, v118
	v_rcp_f32_e32 v119, v119
	v_rcp_f32_e32 v120, v120
	v_rcp_f32_e32 v121, v121
	v_rcp_f32_e32 v122, v122
	v_rcp_f32_e32 v123, v123
	v_rcp_f32_e32 v124, v124
	v_rcp_f32_e32 v125, v125
	v_rcp_f32_e32 v126, v126
	v_rcp_f32_e32 v127, v127
	v_rcp_f32_e32 v128, v128
	v_rcp_f32_e32 v129, v129
	v_rcp_f32_e32 v130, v130
	v_rcp_f32_e32 v131, v131
	v_rcp_f32_e32 v132, v132
	v_rcp_f32_e32 v133, v133
	v_pk_fma_f32 v[118:119], v[118:119], s[6:7], 0.5 op_sel_hi:[1,0,0]
	v_pk_fma_f32 v[120:121], v[120:121], s[6:7], 0.5 op_sel_hi:[1,0,0]
	v_pk_fma_f32 v[122:123], v[122:123], s[6:7], 0.5 op_sel_hi:[1,0,0]
	v_pk_fma_f32 v[124:125], v[124:125], s[6:7], 0.5 op_sel_hi:[1,0,0]
	v_pk_fma_f32 v[126:127], v[126:127], s[6:7], 0.5 op_sel_hi:[1,0,0]
	v_pk_fma_f32 v[128:129], v[128:129], s[6:7], 0.5 op_sel_hi:[1,0,0]
	v_pk_fma_f32 v[130:131], v[130:131], s[6:7], 0.5 op_sel_hi:[1,0,0]
	v_pk_fma_f32 v[132:133], v[132:133], s[6:7], 0.5 op_sel_hi:[1,0,0]
	v_cvt_u32_f32_e32 v126, v126
	v_cvt_u32_f32_e32 v127, v127
	v_cvt_u32_f32_sdwa v128, v128 dst_sel:WORD_1 dst_unused:UNUSED_PAD src0_sel:DWORD
	v_cvt_u32_f32_sdwa v129, v129 dst_sel:BYTE_3 dst_unused:UNUSED_PAD src0_sel:DWORD
	v_cvt_u32_f32_e32 v118, v118
	v_cvt_u32_f32_e32 v119, v119
	v_cvt_u32_f32_sdwa v120, v120 dst_sel:WORD_1 dst_unused:UNUSED_PAD src0_sel:DWORD
	v_cvt_u32_f32_sdwa v121, v121 dst_sel:BYTE_3 dst_unused:UNUSED_PAD src0_sel:DWORD
; DI float sigmoid64_(float x64) { return __builtin_amdgcn_rcpf(1.0f + __builtin_amdgcn_exp2f(x64 * (-LOG2E * W8_INV))); }
;     DI void operator()(const f32x4 (&acc)[2][2][4][2], const Unit& u, int wr, int wc, int fr, int fq) const {
;     ...
;             else {
; #pragma unroll
;                 for (int ai = 0; ai < 2; ++ai)
; #pragma unroll
;                     for (int m = 0; m < 4; ++m) { unsigned char* rowp = (unsigned char*)gt + (size_t)(row0 + ai * 128 + m * 16) * 2048 + (pn - 30) * 256 + wc * 32 + 8 * fq;
;                         u32x2 o[2];
; #pragma unroll
;                         for (int bj = 0; bj < 2; ++bj) {
; #pragma unroll
;                             for (int n = 0; n < 2; ++n) { const f32x4 v = acc[ai][bj][m][n];
;                                 o[bj][n] = (unsigned)(sigmoid64_(v[0]) * 255.0f + 0.5f) | ((unsigned)(sigmoid64_(v[1]) * 255.0f + 0.5f) << 8) | ((unsigned)(sigmoid64_(v[2]) * 255.0f + 0.5f) << 16) | ((unsigned)(sigmoid64_(v[3]) * 255.0f + 0.5f) << 24); } }
;                         st_pair16(rowp, 128, o[0], o[1], fq); }
;                 return; }
	v_cvt_u32_f32_e32 v130, v130
	v_cvt_u32_f32_e32 v131, v131
	v_cvt_u32_f32_sdwa v132, v132 dst_sel:WORD_1 dst_unused:UNUSED_PAD src0_sel:DWORD
	v_cvt_u32_f32_sdwa v133, v133 dst_sel:BYTE_3 dst_unused:UNUSED_PAD src0_sel:DWORD
	v_cvt_u32_f32_e32 v122, v122
	v_cvt_u32_f32_e32 v123, v123
	v_cvt_u32_f32_sdwa v124, v124 dst_sel:WORD_1 dst_unused:UNUSED_PAD src0_sel:DWORD
	v_cvt_u32_f32_sdwa v125, v125 dst_sel:BYTE_3 dst_unused:UNUSED_PAD src0_sel:DWORD
	v_lshl_or_b32 v126, v127, 8, v126
	v_lshl_or_b32 v118, v119, 8, v118
	v_lshl_or_b32 v130, v131, 8, v130
	v_lshl_or_b32 v122, v123, 8, v122
	v_or3_b32 v126, v126, v128, v129
	v_or3_b32 v127, v118, v120, v121
	v_or3_b32 v128, v130, v132, v133
	v_or3_b32 v129, v122, v124, v125
	v_add_co_u32_e32 v14, vcc, 0x10000, v12
	s_nop 0
	v_permlane16_swap_b32_e32 v126, v128
	v_addc_co_u32_e32 v15, vcc, 0, v13, vcc
	v_permlane16_swap_b32_e32 v127, v129
	global_store_dwordx4 v[14:15], v[126:129], off
	v_pk_mul_f32 v[102:103], v[102:103], s[4:5] op_sel_hi:[1,0]
	v_pk_mul_f32 v[104:105], v[104:105], s[4:5] op_sel_hi:[1,0]
	v_pk_mul_f32 v[106:107], v[106:107], s[4:5] op_sel_hi:[1,0]
	v_pk_mul_f32 v[108:109], v[108:109], s[4:5] op_sel_hi:[1,0]
	v_pk_mul_f32 v[110:111], v[110:111], s[4:5] op_sel_hi:[1,0]
	v_pk_mul_f32 v[112:113], v[112:113], s[4:5] op_sel_hi:[1,0]
	v_pk_mul_f32 v[114:115], v[114:115], s[4:5] op_sel_hi:[1,0]
	v_pk_mul_f32 v[116:117], v[116:117], s[4:5] op_sel_hi:[1,0]
	v_exp_f32_e32 v102, v102
	v_exp_f32_e32 v103, v103
	v_exp_f32_e32 v104, v104
	v_exp_f32_e32 v105, v105
	v_exp_f32_e32 v106, v106
	v_exp_f32_e32 v107, v107
	v_exp_f32_e32 v108, v108
	v_exp_f32_e32 v109, v109
	v_exp_f32_e32 v110, v110
	v_exp_f32_e32 v111, v111
	v_exp_f32_e32 v112, v112
	v_exp_f32_e32 v113, v113
	v_exp_f32_e32 v114, v114
	v_exp_f32_e32 v115, v115
	v_exp_f32_e32 v116, v116
	v_exp_f32_e32 v117, v117
	v_pk_add_f32 v[102:103], v[102:103], 1.0 op_sel_hi:[1,0]
	v_pk_add_f32 v[104:105], v[104:105], 1.0 op_sel_hi:[1,0]
	v_pk_add_f32 v[106:107], v[106:107], 1.0 op_sel_hi:[1,0]
	v_pk_add_f32 v[108:109], v[108:109], 1.0 op_sel_hi:[1,0]
	v_pk_add_f32 v[110:111], v[110:111], 1.0 op_sel_hi:[1,0]
	v_pk_add_f32 v[112:113], v[112:113], 1.0 op_sel_hi:[1,0]
	v_pk_add_f32 v[114:115], v[114:115], 1.0 op_sel_hi:[1,0]
	v_pk_add_f32 v[116:117], v[116:117], 1.0 op_sel_hi:[1,0]
	v_rcp_f32_e32 v102, v102
	v_rcp_f32_e32 v103, v103
	v_rcp_f32_e32 v104, v104
	v_rcp_f32_e32 v105, v105
	v_rcp_f32_e32 v106, v106
	v_rcp_f32_e32 v107, v107
	v_rcp_f32_e32 v108, v108
	v_rcp_f32_e32 v109, v109
	v_rcp_f32_e32 v110, v110
	v_rcp_f32_e32 v111, v111
	v_rcp_f32_e32 v112, v112
	v_rcp_f32_e32 v113, v113
	v_rcp_f32_e32 v114, v114
	v_rcp_f32_e32 v115, v115
	v_rcp_f32_e32 v116, v116
	v_rcp_f32_e32 v117, v117
	v_pk_fma_f32 v[102:103], v[102:103], s[6:7], 0.5 op_sel_hi:[1,0,0]
	v_pk_fma_f32 v[104:105], v[104:105], s[6:7], 0.5 op_sel_hi:[1,0,0]
	v_pk_fma_f32 v[106:107], v[106:107], s[6:7], 0.5 op_sel_hi:[1,0,0]
	v_pk_fma_f32 v[108:109], v[108:109], s[6:7], 0.5 op_sel_hi:[1,0,0]
	v_pk_fma_f32 v[110:111], v[110:111], s[6:7], 0.5 op_sel_hi:[1,0,0]
	v_pk_fma_f32 v[112:113], v[112:113], s[6:7], 0.5 op_sel_hi:[1,0,0]
	v_pk_fma_f32 v[114:115], v[114:115], s[6:7], 0.5 op_sel_hi:[1,0,0]
	v_pk_fma_f32 v[116:117], v[116:117], s[6:7], 0.5 op_sel_hi:[1,0,0]
	v_cvt_u32_f32_e32 v110, v110
	v_cvt_u32_f32_e32 v111, v111
	v_cvt_u32_f32_sdwa v112, v112 dst_sel:WORD_1 dst_unused:UNUSED_PAD src0_sel:DWORD
	v_cvt_u32_f32_sdwa v113, v113 dst_sel:BYTE_3 dst_unused:UNUSED_PAD src0_sel:DWORD
	v_cvt_u32_f32_e32 v102, v102
	v_cvt_u32_f32_e32 v103, v103
	v_cvt_u32_f32_sdwa v104, v104 dst_sel:WORD_1 dst_unused:UNUSED_PAD src0_sel:DWORD
	v_cvt_u32_f32_sdwa v105, v105 dst_sel:BYTE_3 dst_unused:UNUSED_PAD src0_sel:DWORD
	v_cvt_u32_f32_e32 v114, v114
	v_cvt_u32_f32_e32 v115, v115
	v_cvt_u32_f32_sdwa v116, v116 dst_sel:WORD_1 dst_unused:UNUSED_PAD src0_sel:DWORD
	v_cvt_u32_f32_sdwa v117, v117 dst_sel:BYTE_3 dst_unused:UNUSED_PAD src0_sel:DWORD
	v_cvt_u32_f32_e32 v106, v106
	v_cvt_u32_f32_e32 v107, v107
	v_cvt_u32_f32_sdwa v108, v108 dst_sel:WORD_1 dst_unused:UNUSED_PAD src0_sel:DWORD
	v_cvt_u32_f32_sdwa v109, v109 dst_sel:BYTE_3 dst_unused:UNUSED_PAD src0_sel:DWORD
	v_lshl_or_b32 v110, v111, 8, v110
	v_lshl_or_b32 v102, v103, 8, v102
	v_lshl_or_b32 v114, v115, 8, v114
	v_lshl_or_b32 v106, v107, 8, v106
	v_or3_b32 v110, v110, v112, v113
	v_or3_b32 v111, v102, v104, v105
	v_or3_b32 v112, v114, v116, v117
	v_or3_b32 v113, v106, v108, v109
	v_add_co_u32_e32 v14, vcc, 0x18000, v12
	s_nop 0
	v_permlane16_swap_b32_e32 v110, v112
	v_addc_co_u32_e32 v15, vcc, 0, v13, vcc
	v_permlane16_swap_b32_e32 v111, v113
	global_store_dwordx4 v[14:15], v[110:113], off
	v_pk_mul_f32 v[86:87], v[86:87], s[4:5] op_sel_hi:[1,0]
	v_pk_mul_f32 v[88:89], v[88:89], s[4:5] op_sel_hi:[1,0]
	v_pk_mul_f32 v[90:91], v[90:91], s[4:5] op_sel_hi:[1,0]
	v_pk_mul_f32 v[92:93], v[92:93], s[4:5] op_sel_hi:[1,0]
	v_pk_mul_f32 v[94:95], v[94:95], s[4:5] op_sel_hi:[1,0]
	v_pk_mul_f32 v[96:97], v[96:97], s[4:5] op_sel_hi:[1,0]
	v_pk_mul_f32 v[98:99], v[98:99], s[4:5] op_sel_hi:[1,0]
	v_pk_mul_f32 v[100:101], v[100:101], s[4:5] op_sel_hi:[1,0]
	v_exp_f32_e32 v86, v86
	v_exp_f32_e32 v87, v87
	v_exp_f32_e32 v88, v88
	v_exp_f32_e32 v89, v89
	v_exp_f32_e32 v90, v90
	v_exp_f32_e32 v91, v91
	v_exp_f32_e32 v92, v92
	v_exp_f32_e32 v93, v93
	v_exp_f32_e32 v94, v94
	v_exp_f32_e32 v95, v95
	v_exp_f32_e32 v96, v96
	v_exp_f32_e32 v97, v97
	v_exp_f32_e32 v98, v98
	v_exp_f32_e32 v99, v99
	v_exp_f32_e32 v100, v100
	v_exp_f32_e32 v101, v101
	v_pk_add_f32 v[86:87], v[86:87], 1.0 op_sel_hi:[1,0]
	v_pk_add_f32 v[88:89], v[88:89], 1.0 op_sel_hi:[1,0]
; DI float sigmoid64_(float x64) { return __builtin_amdgcn_rcpf(1.0f + __builtin_amdgcn_exp2f(x64 * (-LOG2E * W8_INV))); }
;     DI void operator()(const f32x4 (&acc)[2][2][4][2], const Unit& u, int wr, int wc, int fr, int fq) const {
;     ...
;             else {
; #pragma unroll
;                 for (int ai = 0; ai < 2; ++ai)
; #pragma unroll
;                     for (int m = 0; m < 4; ++m) { unsigned char* rowp = (unsigned char*)gt + (size_t)(row0 + ai * 128 + m * 16) * 2048 + (pn - 30) * 256 + wc * 32 + 8 * fq;
;                         u32x2 o[2];
; #pragma unroll
;                         for (int bj = 0; bj < 2; ++bj) {
; #pragma unroll
;                             for (int n = 0; n < 2; ++n) { const f32x4 v = acc[ai][bj][m][n];
;                                 o[bj][n] = (unsigned)(sigmoid64_(v[0]) * 255.0f + 0.5f) | ((unsigned)(sigmoid64_(v[1]) * 255.0f + 0.5f) << 8) | ((unsigned)(sigmoid64_(v[2]) * 255.0f + 0.5f) << 16) | ((unsigned)(sigmoid64_(v[3]) * 255.0f + 0.5f) << 24); } }
;                         st_pair16(rowp, 128, o[0], o[1], fq); }
;                 return; }
	v_pk_add_f32 v[90:91], v[90:91], 1.0 op_sel_hi:[1,0]
	v_pk_add_f32 v[92:93], v[92:93], 1.0 op_sel_hi:[1,0]
	v_pk_add_f32 v[94:95], v[94:95], 1.0 op_sel_hi:[1,0]
	v_pk_add_f32 v[96:97], v[96:97], 1.0 op_sel_hi:[1,0]
	v_pk_add_f32 v[98:99], v[98:99], 1.0 op_sel_hi:[1,0]
	v_pk_add_f32 v[100:101], v[100:101], 1.0 op_sel_hi:[1,0]
	v_rcp_f32_e32 v86, v86
	v_rcp_f32_e32 v87, v87
	v_rcp_f32_e32 v88, v88
	v_rcp_f32_e32 v89, v89
	v_rcp_f32_e32 v90, v90
	v_rcp_f32_e32 v91, v91
	v_rcp_f32_e32 v92, v92
	v_rcp_f32_e32 v93, v93
	v_rcp_f32_e32 v94, v94
	v_rcp_f32_e32 v95, v95
	v_rcp_f32_e32 v96, v96
	v_rcp_f32_e32 v97, v97
	v_rcp_f32_e32 v98, v98
	v_rcp_f32_e32 v99, v99
	v_rcp_f32_e32 v100, v100
	v_rcp_f32_e32 v101, v101
	v_pk_fma_f32 v[86:87], v[86:87], s[6:7], 0.5 op_sel_hi:[1,0,0]
	v_pk_fma_f32 v[88:89], v[88:89], s[6:7], 0.5 op_sel_hi:[1,0,0]
	v_pk_fma_f32 v[90:91], v[90:91], s[6:7], 0.5 op_sel_hi:[1,0,0]
	v_pk_fma_f32 v[92:93], v[92:93], s[6:7], 0.5 op_sel_hi:[1,0,0]
	v_pk_fma_f32 v[94:95], v[94:95], s[6:7], 0.5 op_sel_hi:[1,0,0]
	v_pk_fma_f32 v[96:97], v[96:97], s[6:7], 0.5 op_sel_hi:[1,0,0]
	v_pk_fma_f32 v[98:99], v[98:99], s[6:7], 0.5 op_sel_hi:[1,0,0]
	v_pk_fma_f32 v[100:101], v[100:101], s[6:7], 0.5 op_sel_hi:[1,0,0]
	v_cvt_u32_f32_e32 v94, v94
	v_cvt_u32_f32_e32 v95, v95
	v_cvt_u32_f32_sdwa v96, v96 dst_sel:WORD_1 dst_unused:UNUSED_PAD src0_sel:DWORD
	v_cvt_u32_f32_sdwa v97, v97 dst_sel:BYTE_3 dst_unused:UNUSED_PAD src0_sel:DWORD
	v_cvt_u32_f32_e32 v86, v86
	v_cvt_u32_f32_e32 v87, v87
	v_cvt_u32_f32_sdwa v88, v88 dst_sel:WORD_1 dst_unused:UNUSED_PAD src0_sel:DWORD
	v_cvt_u32_f32_sdwa v89, v89 dst_sel:BYTE_3 dst_unused:UNUSED_PAD src0_sel:DWORD
	v_cvt_u32_f32_e32 v98, v98
	v_cvt_u32_f32_e32 v99, v99
	v_cvt_u32_f32_sdwa v100, v100 dst_sel:WORD_1 dst_unused:UNUSED_PAD src0_sel:DWORD
	v_cvt_u32_f32_sdwa v101, v101 dst_sel:BYTE_3 dst_unused:UNUSED_PAD src0_sel:DWORD
	v_cvt_u32_f32_e32 v90, v90
	v_cvt_u32_f32_e32 v91, v91
	v_cvt_u32_f32_sdwa v92, v92 dst_sel:WORD_1 dst_unused:UNUSED_PAD src0_sel:DWORD
	v_cvt_u32_f32_sdwa v93, v93 dst_sel:BYTE_3 dst_unused:UNUSED_PAD src0_sel:DWORD
	v_lshl_or_b32 v94, v95, 8, v94
	v_lshl_or_b32 v86, v87, 8, v86
	v_lshl_or_b32 v98, v99, 8, v98
	v_lshl_or_b32 v90, v91, 8, v90
	v_or3_b32 v94, v94, v96, v97
	v_or3_b32 v95, v86, v88, v89
	v_or3_b32 v96, v98, v100, v101
	v_or3_b32 v97, v90, v92, v93
	v_add_co_u32_e32 v14, vcc, 0x40000, v12
	s_nop 0
	v_permlane16_swap_b32_e32 v94, v96
	v_addc_co_u32_e32 v15, vcc, 0, v13, vcc
	v_permlane16_swap_b32_e32 v95, v97
	global_store_dwordx4 v[14:15], v[94:97], off
	v_pk_mul_f32 v[70:71], v[70:71], s[4:5] op_sel_hi:[1,0]
	v_pk_mul_f32 v[72:73], v[72:73], s[4:5] op_sel_hi:[1,0]
	v_pk_mul_f32 v[74:75], v[74:75], s[4:5] op_sel_hi:[1,0]
	v_pk_mul_f32 v[76:77], v[76:77], s[4:5] op_sel_hi:[1,0]
	v_pk_mul_f32 v[78:79], v[78:79], s[4:5] op_sel_hi:[1,0]
	v_pk_mul_f32 v[80:81], v[80:81], s[4:5] op_sel_hi:[1,0]
	v_pk_mul_f32 v[82:83], v[82:83], s[4:5] op_sel_hi:[1,0]
	v_pk_mul_f32 v[84:85], v[84:85], s[4:5] op_sel_hi:[1,0]
	v_exp_f32_e32 v70, v70
	v_exp_f32_e32 v71, v71
	v_exp_f32_e32 v72, v72
	v_exp_f32_e32 v73, v73
	v_exp_f32_e32 v74, v74
	v_exp_f32_e32 v75, v75
	v_exp_f32_e32 v76, v76
	v_exp_f32_e32 v77, v77
	v_exp_f32_e32 v78, v78
	v_exp_f32_e32 v79, v79
	v_exp_f32_e32 v80, v80
	v_exp_f32_e32 v81, v81
	v_exp_f32_e32 v82, v82
	v_exp_f32_e32 v83, v83
	v_exp_f32_e32 v84, v84
	v_exp_f32_e32 v85, v85
	v_pk_add_f32 v[70:71], v[70:71], 1.0 op_sel_hi:[1,0]
	v_pk_add_f32 v[72:73], v[72:73], 1.0 op_sel_hi:[1,0]
	v_pk_add_f32 v[74:75], v[74:75], 1.0 op_sel_hi:[1,0]
	v_pk_add_f32 v[76:77], v[76:77], 1.0 op_sel_hi:[1,0]
	v_pk_add_f32 v[78:79], v[78:79], 1.0 op_sel_hi:[1,0]
	v_pk_add_f32 v[80:81], v[80:81], 1.0 op_sel_hi:[1,0]
	v_pk_add_f32 v[82:83], v[82:83], 1.0 op_sel_hi:[1,0]
	v_pk_add_f32 v[84:85], v[84:85], 1.0 op_sel_hi:[1,0]
	v_rcp_f32_e32 v70, v70
	v_rcp_f32_e32 v71, v71
	v_rcp_f32_e32 v72, v72
	v_rcp_f32_e32 v73, v73
	v_rcp_f32_e32 v74, v74
	v_rcp_f32_e32 v75, v75
	v_rcp_f32_e32 v76, v76
	v_rcp_f32_e32 v77, v77
	v_rcp_f32_e32 v78, v78
	v_rcp_f32_e32 v79, v79
	v_rcp_f32_e32 v80, v80
	v_rcp_f32_e32 v81, v81
	v_rcp_f32_e32 v82, v82
	v_rcp_f32_e32 v83, v83
	v_rcp_f32_e32 v84, v84
	v_rcp_f32_e32 v85, v85
	v_pk_fma_f32 v[70:71], v[70:71], s[6:7], 0.5 op_sel_hi:[1,0,0]
	v_pk_fma_f32 v[72:73], v[72:73], s[6:7], 0.5 op_sel_hi:[1,0,0]
	v_pk_fma_f32 v[74:75], v[74:75], s[6:7], 0.5 op_sel_hi:[1,0,0]
	v_pk_fma_f32 v[76:77], v[76:77], s[6:7], 0.5 op_sel_hi:[1,0,0]
	v_pk_fma_f32 v[78:79], v[78:79], s[6:7], 0.5 op_sel_hi:[1,0,0]
	v_pk_fma_f32 v[80:81], v[80:81], s[6:7], 0.5 op_sel_hi:[1,0,0]
	v_pk_fma_f32 v[82:83], v[82:83], s[6:7], 0.5 op_sel_hi:[1,0,0]
	v_pk_fma_f32 v[84:85], v[84:85], s[6:7], 0.5 op_sel_hi:[1,0,0]
	v_cvt_u32_f32_e32 v78, v78
	v_cvt_u32_f32_e32 v79, v79
	v_cvt_u32_f32_sdwa v80, v80 dst_sel:WORD_1 dst_unused:UNUSED_PAD src0_sel:DWORD
	v_cvt_u32_f32_sdwa v81, v81 dst_sel:BYTE_3 dst_unused:UNUSED_PAD src0_sel:DWORD
	v_cvt_u32_f32_e32 v70, v70
	v_cvt_u32_f32_e32 v71, v71
	v_cvt_u32_f32_sdwa v72, v72 dst_sel:WORD_1 dst_unused:UNUSED_PAD src0_sel:DWORD
	v_cvt_u32_f32_sdwa v73, v73 dst_sel:BYTE_3 dst_unused:UNUSED_PAD src0_sel:DWORD
	v_cvt_u32_f32_e32 v82, v82
	v_cvt_u32_f32_e32 v83, v83
	v_cvt_u32_f32_sdwa v84, v84 dst_sel:WORD_1 dst_unused:UNUSED_PAD src0_sel:DWORD
	v_cvt_u32_f32_sdwa v85, v85 dst_sel:BYTE_3 dst_unused:UNUSED_PAD src0_sel:DWORD
	v_cvt_u32_f32_e32 v74, v74
	v_cvt_u32_f32_e32 v75, v75
	v_cvt_u32_f32_sdwa v76, v76 dst_sel:WORD_1 dst_unused:UNUSED_PAD src0_sel:DWORD
	v_cvt_u32_f32_sdwa v77, v77 dst_sel:BYTE_3 dst_unused:UNUSED_PAD src0_sel:DWORD
	v_lshl_or_b32 v78, v79, 8, v78
; DI float sigmoid64_(float x64) { return __builtin_amdgcn_rcpf(1.0f + __builtin_amdgcn_exp2f(x64 * (-LOG2E * W8_INV))); }
;     DI void operator()(const f32x4 (&acc)[2][2][4][2], const Unit& u, int wr, int wc, int fr, int fq) const {
;     ...
;             else {
; #pragma unroll
;                 for (int ai = 0; ai < 2; ++ai)
; #pragma unroll
;                     for (int m = 0; m < 4; ++m) { unsigned char* rowp = (unsigned char*)gt + (size_t)(row0 + ai * 128 + m * 16) * 2048 + (pn - 30) * 256 + wc * 32 + 8 * fq;
;                         u32x2 o[2];
; #pragma unroll
;                         for (int bj = 0; bj < 2; ++bj) {
; #pragma unroll
;                             for (int n = 0; n < 2; ++n) { const f32x4 v = acc[ai][bj][m][n];
;                                 o[bj][n] = (unsigned)(sigmoid64_(v[0]) * 255.0f + 0.5f) | ((unsigned)(sigmoid64_(v[1]) * 255.0f + 0.5f) << 8) | ((unsigned)(sigmoid64_(v[2]) * 255.0f + 0.5f) << 16) | ((unsigned)(sigmoid64_(v[3]) * 255.0f + 0.5f) << 24); } }
;                         st_pair16(rowp, 128, o[0], o[1], fq); }
;                 return; }
	v_lshl_or_b32 v70, v71, 8, v70
	v_lshl_or_b32 v82, v83, 8, v82
	v_lshl_or_b32 v74, v75, 8, v74
	v_or3_b32 v78, v78, v80, v81
	v_or3_b32 v79, v70, v72, v73
	v_or3_b32 v80, v82, v84, v85
	v_or3_b32 v81, v74, v76, v77
	v_add_co_u32_e32 v14, vcc, 0x48000, v12
	s_nop 0
	v_permlane16_swap_b32_e32 v78, v80
	v_addc_co_u32_e32 v15, vcc, 0, v13, vcc
	v_permlane16_swap_b32_e32 v79, v81
	global_store_dwordx4 v[14:15], v[78:81], off
	v_pk_mul_f32 v[54:55], v[54:55], s[4:5] op_sel_hi:[1,0]
	v_pk_mul_f32 v[56:57], v[56:57], s[4:5] op_sel_hi:[1,0]
	v_pk_mul_f32 v[58:59], v[58:59], s[4:5] op_sel_hi:[1,0]
	v_pk_mul_f32 v[60:61], v[60:61], s[4:5] op_sel_hi:[1,0]
	v_pk_mul_f32 v[62:63], v[62:63], s[4:5] op_sel_hi:[1,0]
	v_pk_mul_f32 v[64:65], v[64:65], s[4:5] op_sel_hi:[1,0]
	v_pk_mul_f32 v[66:67], v[66:67], s[4:5] op_sel_hi:[1,0]
	v_pk_mul_f32 v[68:69], v[68:69], s[4:5] op_sel_hi:[1,0]
	v_exp_f32_e32 v54, v54
	v_exp_f32_e32 v55, v55
	v_exp_f32_e32 v56, v56
	v_exp_f32_e32 v57, v57
	v_exp_f32_e32 v58, v58
	v_exp_f32_e32 v59, v59
	v_exp_f32_e32 v60, v60
	v_exp_f32_e32 v61, v61
	v_exp_f32_e32 v62, v62
	v_exp_f32_e32 v63, v63
	v_exp_f32_e32 v64, v64
	v_exp_f32_e32 v65, v65
	v_exp_f32_e32 v66, v66
	v_exp_f32_e32 v67, v67
	v_exp_f32_e32 v68, v68
	v_exp_f32_e32 v69, v69
	v_pk_add_f32 v[54:55], v[54:55], 1.0 op_sel_hi:[1,0]
	v_pk_add_f32 v[56:57], v[56:57], 1.0 op_sel_hi:[1,0]
	v_pk_add_f32 v[58:59], v[58:59], 1.0 op_sel_hi:[1,0]
	v_pk_add_f32 v[60:61], v[60:61], 1.0 op_sel_hi:[1,0]
	v_pk_add_f32 v[62:63], v[62:63], 1.0 op_sel_hi:[1,0]
	v_pk_add_f32 v[64:65], v[64:65], 1.0 op_sel_hi:[1,0]
	v_pk_add_f32 v[66:67], v[66:67], 1.0 op_sel_hi:[1,0]
	v_pk_add_f32 v[68:69], v[68:69], 1.0 op_sel_hi:[1,0]
	v_rcp_f32_e32 v54, v54
	v_rcp_f32_e32 v55, v55
	v_rcp_f32_e32 v56, v56
	v_rcp_f32_e32 v57, v57
	v_rcp_f32_e32 v58, v58
	v_rcp_f32_e32 v59, v59
	v_rcp_f32_e32 v60, v60
	v_rcp_f32_e32 v61, v61
	v_rcp_f32_e32 v62, v62
	v_rcp_f32_e32 v63, v63
	v_rcp_f32_e32 v64, v64
	v_rcp_f32_e32 v65, v65
	v_rcp_f32_e32 v66, v66
	v_rcp_f32_e32 v67, v67
	v_rcp_f32_e32 v68, v68
	v_rcp_f32_e32 v69, v69
	v_pk_fma_f32 v[54:55], v[54:55], s[6:7], 0.5 op_sel_hi:[1,0,0]
	v_pk_fma_f32 v[56:57], v[56:57], s[6:7], 0.5 op_sel_hi:[1,0,0]
	v_pk_fma_f32 v[58:59], v[58:59], s[6:7], 0.5 op_sel_hi:[1,0,0]
	v_pk_fma_f32 v[60:61], v[60:61], s[6:7], 0.5 op_sel_hi:[1,0,0]
	v_pk_fma_f32 v[62:63], v[62:63], s[6:7], 0.5 op_sel_hi:[1,0,0]
	v_pk_fma_f32 v[64:65], v[64:65], s[6:7], 0.5 op_sel_hi:[1,0,0]
	v_pk_fma_f32 v[66:67], v[66:67], s[6:7], 0.5 op_sel_hi:[1,0,0]
	v_pk_fma_f32 v[68:69], v[68:69], s[6:7], 0.5 op_sel_hi:[1,0,0]
	v_cvt_u32_f32_e32 v62, v62
	v_cvt_u32_f32_e32 v63, v63
	v_cvt_u32_f32_sdwa v64, v64 dst_sel:WORD_1 dst_unused:UNUSED_PAD src0_sel:DWORD
	v_cvt_u32_f32_sdwa v65, v65 dst_sel:BYTE_3 dst_unused:UNUSED_PAD src0_sel:DWORD
	v_cvt_u32_f32_e32 v54, v54
	v_cvt_u32_f32_e32 v55, v55
	v_cvt_u32_f32_sdwa v56, v56 dst_sel:WORD_1 dst_unused:UNUSED_PAD src0_sel:DWORD
	v_cvt_u32_f32_sdwa v57, v57 dst_sel:BYTE_3 dst_unused:UNUSED_PAD src0_sel:DWORD
	v_cvt_u32_f32_e32 v66, v66
	v_cvt_u32_f32_e32 v67, v67
	v_cvt_u32_f32_sdwa v68, v68 dst_sel:WORD_1 dst_unused:UNUSED_PAD src0_sel:DWORD
	v_cvt_u32_f32_sdwa v69, v69 dst_sel:BYTE_3 dst_unused:UNUSED_PAD src0_sel:DWORD
	v_cvt_u32_f32_e32 v58, v58
	v_cvt_u32_f32_e32 v59, v59
	v_cvt_u32_f32_sdwa v60, v60 dst_sel:WORD_1 dst_unused:UNUSED_PAD src0_sel:DWORD
	v_cvt_u32_f32_sdwa v61, v61 dst_sel:BYTE_3 dst_unused:UNUSED_PAD src0_sel:DWORD
	v_lshl_or_b32 v62, v63, 8, v62
	v_lshl_or_b32 v54, v55, 8, v54
	v_lshl_or_b32 v66, v67, 8, v66
	v_lshl_or_b32 v58, v59, 8, v58
	v_or3_b32 v62, v62, v64, v65
	v_or3_b32 v63, v54, v56, v57
	v_or3_b32 v64, v66, v68, v69
	v_or3_b32 v65, v58, v60, v61
; DI float sigmoid64_(float x64) { return __builtin_amdgcn_rcpf(1.0f + __builtin_amdgcn_exp2f(x64 * (-LOG2E * W8_INV))); }
;     DI void operator()(const f32x4 (&acc)[2][2][4][2], const Unit& u, int wr, int wc, int fr, int fq) const {
;     ...
;             else {
; #pragma unroll
;                 for (int ai = 0; ai < 2; ++ai)
; #pragma unroll
;                     for (int m = 0; m < 4; ++m) { unsigned char* rowp = (unsigned char*)gt + (size_t)(row0 + ai * 128 + m * 16) * 2048 + (pn - 30) * 256 + wc * 32 + 8 * fq;
;                         u32x2 o[2];
; #pragma unroll
;                         for (int bj = 0; bj < 2; ++bj) {
; #pragma unroll
;                             for (int n = 0; n < 2; ++n) { const f32x4 v = acc[ai][bj][m][n];
;                                 o[bj][n] = (unsigned)(sigmoid64_(v[0]) * 255.0f + 0.5f) | ((unsigned)(sigmoid64_(v[1]) * 255.0f + 0.5f) << 8) | ((unsigned)(sigmoid64_(v[2]) * 255.0f + 0.5f) << 16) | ((unsigned)(sigmoid64_(v[3]) * 255.0f + 0.5f) << 24); } }
;                         st_pair16(rowp, 128, o[0], o[1], fq); }
;                 return; }
	v_add_co_u32_e32 v14, vcc, 0x50000, v12
	s_nop 0
	v_permlane16_swap_b32_e32 v62, v64
	v_addc_co_u32_e32 v15, vcc, 0, v13, vcc
	v_permlane16_swap_b32_e32 v63, v65
	global_store_dwordx4 v[14:15], v[62:65], off
	v_pk_mul_f32 v[38:39], v[38:39], s[4:5] op_sel_hi:[1,0]
	v_pk_mul_f32 v[40:41], v[40:41], s[4:5] op_sel_hi:[1,0]
	v_pk_mul_f32 v[42:43], v[42:43], s[4:5] op_sel_hi:[1,0]
	v_pk_mul_f32 v[44:45], v[44:45], s[4:5] op_sel_hi:[1,0]
	v_pk_mul_f32 v[46:47], v[46:47], s[4:5] op_sel_hi:[1,0]
	v_pk_mul_f32 v[48:49], v[48:49], s[4:5] op_sel_hi:[1,0]
	v_pk_mul_f32 v[50:51], v[50:51], s[4:5] op_sel_hi:[1,0]
	v_pk_mul_f32 v[52:53], v[52:53], s[4:5] op_sel_hi:[1,0]
	v_exp_f32_e32 v38, v38
	v_exp_f32_e32 v39, v39
	v_exp_f32_e32 v40, v40
	v_exp_f32_e32 v41, v41
	v_exp_f32_e32 v42, v42
	v_exp_f32_e32 v43, v43
	v_exp_f32_e32 v44, v44
	v_exp_f32_e32 v45, v45
	v_exp_f32_e32 v46, v46
	v_exp_f32_e32 v47, v47
	v_exp_f32_e32 v48, v48
	v_exp_f32_e32 v49, v49
	v_exp_f32_e32 v50, v50
	v_exp_f32_e32 v51, v51
	v_exp_f32_e32 v52, v52
	v_exp_f32_e32 v53, v53
	v_pk_add_f32 v[38:39], v[38:39], 1.0 op_sel_hi:[1,0]
	v_pk_add_f32 v[40:41], v[40:41], 1.0 op_sel_hi:[1,0]
	v_pk_add_f32 v[42:43], v[42:43], 1.0 op_sel_hi:[1,0]
	v_pk_add_f32 v[44:45], v[44:45], 1.0 op_sel_hi:[1,0]
	v_pk_add_f32 v[46:47], v[46:47], 1.0 op_sel_hi:[1,0]
	v_pk_add_f32 v[48:49], v[48:49], 1.0 op_sel_hi:[1,0]
	v_pk_add_f32 v[50:51], v[50:51], 1.0 op_sel_hi:[1,0]
	v_pk_add_f32 v[52:53], v[52:53], 1.0 op_sel_hi:[1,0]
	v_rcp_f32_e32 v38, v38
	v_rcp_f32_e32 v39, v39
	v_rcp_f32_e32 v40, v40
	v_rcp_f32_e32 v41, v41
	v_rcp_f32_e32 v42, v42
	v_rcp_f32_e32 v43, v43
	v_rcp_f32_e32 v44, v44
	v_rcp_f32_e32 v45, v45
	v_rcp_f32_e32 v46, v46
	v_rcp_f32_e32 v47, v47
	v_rcp_f32_e32 v48, v48
	v_rcp_f32_e32 v49, v49
	v_rcp_f32_e32 v50, v50
	v_rcp_f32_e32 v51, v51
	v_rcp_f32_e32 v52, v52
	v_rcp_f32_e32 v53, v53
	v_pk_fma_f32 v[38:39], v[38:39], s[6:7], 0.5 op_sel_hi:[1,0,0]
	v_pk_fma_f32 v[40:41], v[40:41], s[6:7], 0.5 op_sel_hi:[1,0,0]
	v_pk_fma_f32 v[42:43], v[42:43], s[6:7], 0.5 op_sel_hi:[1,0,0]
	v_pk_fma_f32 v[44:45], v[44:45], s[6:7], 0.5 op_sel_hi:[1,0,0]
	v_pk_fma_f32 v[46:47], v[46:47], s[6:7], 0.5 op_sel_hi:[1,0,0]
	v_pk_fma_f32 v[48:49], v[48:49], s[6:7], 0.5 op_sel_hi:[1,0,0]
	v_pk_fma_f32 v[50:51], v[50:51], s[6:7], 0.5 op_sel_hi:[1,0,0]
	v_pk_fma_f32 v[52:53], v[52:53], s[6:7], 0.5 op_sel_hi:[1,0,0]
	v_cvt_u32_f32_e32 v46, v46
	v_cvt_u32_f32_e32 v47, v47
	v_cvt_u32_f32_sdwa v48, v48 dst_sel:WORD_1 dst_unused:UNUSED_PAD src0_sel:DWORD
	v_cvt_u32_f32_sdwa v49, v49 dst_sel:BYTE_3 dst_unused:UNUSED_PAD src0_sel:DWORD
	v_cvt_u32_f32_e32 v38, v38
	v_cvt_u32_f32_e32 v39, v39
	v_cvt_u32_f32_sdwa v40, v40 dst_sel:WORD_1 dst_unused:UNUSED_PAD src0_sel:DWORD
	v_cvt_u32_f32_sdwa v41, v41 dst_sel:BYTE_3 dst_unused:UNUSED_PAD src0_sel:DWORD
	v_cvt_u32_f32_e32 v50, v50
	v_cvt_u32_f32_e32 v51, v51
	v_cvt_u32_f32_sdwa v52, v52 dst_sel:WORD_1 dst_unused:UNUSED_PAD src0_sel:DWORD
	v_cvt_u32_f32_sdwa v53, v53 dst_sel:BYTE_3 dst_unused:UNUSED_PAD src0_sel:DWORD
	v_cvt_u32_f32_e32 v42, v42
	v_cvt_u32_f32_e32 v43, v43
	v_cvt_u32_f32_sdwa v44, v44 dst_sel:WORD_1 dst_unused:UNUSED_PAD src0_sel:DWORD
	v_cvt_u32_f32_sdwa v45, v45 dst_sel:BYTE_3 dst_unused:UNUSED_PAD src0_sel:DWORD
	v_lshl_or_b32 v46, v47, 8, v46
	v_lshl_or_b32 v38, v39, 8, v38
	v_lshl_or_b32 v50, v51, 8, v50
	v_lshl_or_b32 v42, v43, 8, v42
	v_or3_b32 v46, v46, v48, v49
	v_or3_b32 v47, v38, v40, v41
	v_or3_b32 v48, v50, v52, v53
	v_or3_b32 v49, v42, v44, v45
	v_add_co_u32_e32 v14, vcc, 0x58000, v12
	s_nop 0
	v_permlane16_swap_b32_e32 v46, v48
	v_addc_co_u32_e32 v15, vcc, 0, v13, vcc
	v_permlane16_swap_b32_e32 v47, v49
	global_store_dwordx4 v[14:15], v[46:49], off

; DI unsigned pk4_fp8(float a, float b, float c_, float d) { int w = 0; w = __builtin_amdgcn_cvt_pk_fp8_f32(clamp8(a), clamp8(b), w, false); w = __builtin_amdgcn_cvt_pk_fp8_f32(clamp8(c_), clamp8(d), w, true); return (unsigned)w; }
; DI float sigmoidf_(float x) { return __builtin_amdgcn_rcpf(1.0f + __builtin_amdgcn_exp2f(-x * LOG2E)); }
;     DI void operator()(const f32x4 (&acc)[2][2][4][2], const Unit& u, int wr, int wc, int fr, int fq) const {
;     ...
;             else if (pn < 12) {
; #pragma unroll
;                 for (int ai = 0; ai < 2; ++ai)
; #pragma unroll
;                     for (int m = 0; m < 4; ++m) { unsigned char* rowp = (unsigned char*)sr + (size_t)(row0 + ai * 128 + m * 16) * 1024 + (pn - 8) * 256 + wc * 32 + 8 * fq;
;                         u32x2 o[2];
; #pragma unroll
;                         for (int bj = 0; bj < 2; ++bj) { const f32x4 v0 = acc[ai][bj][m][0] * W8_INV, v1 = acc[ai][bj][m][1] * W8_INV;
;                             o[bj].x = pk4_fp8(v0[0] * sigmoidf_(v0[0]), v0[1] * sigmoidf_(v0[1]), v0[2] * sigmoidf_(v0[2]), v0[3] * sigmoidf_(v0[3]));
;                             o[bj].y = pk4_fp8(v1[0] * sigmoidf_(v1[0]), v1[1] * sigmoidf_(v1[1]), v1[2] * sigmoidf_(v1[2]), v1[3] * sigmoidf_(v1[3])); }
;                         st_pair16(rowp, 128, o[0], o[1], fq); }
;                 return; }
.LBB0_294:
	s_andn2_b64 vcc, exec, s[16:17]
	s_cbranch_vccnz .LBB0_296
	v_bfe_i32 v6, v18, 0, 1
	v_and_b32_e32 v14, 0x78, v6
	v_mov_b32_e32 v15, v4
	v_ashrrev_i32_e32 v11, 31, v10
	v_lshlrev_b64 v[6:7], 10, v[10:11]
	v_readlane_b32 s6, v255, 22
	v_readlane_b32 s7, v255, 23
	s_lshl_b32 s4, s43, 8
	s_addk_i32 s4, 0xf800
	s_ashr_i32 s5, s4, 31
	v_lshl_add_u64 v[6:7], s[6:7], 0, v[6:7]
	v_lshl_add_u64 v[6:7], v[6:7], 0, s[4:5]
	v_readlane_b32 s4, v255, 36
	v_readlane_b32 s5, v255, 37
	v_lshl_add_u64 v[16:17], v[6:7], 0, s[4:5]
	v_lshlrev_b32_e32 v12, 3, v18
	v_ashrrev_i32_e32 v13, 31, v12
	v_lshl_add_u64 v[12:13], v[16:17], 0, v[12:13]
	v_lshl_add_u64 v[12:13], v[12:13], 0, v[14:15]
	s_mov_b32 s4, 0xbfb8aa3b
	v_pk_mul_f32 v[150:151], v[150:151], s[34:35] op_sel_hi:[1,0]
	v_pk_mul_f32 v[152:153], v[152:153], s[34:35] op_sel_hi:[1,0]
	v_pk_mul_f32 v[154:155], v[154:155], s[34:35] op_sel_hi:[1,0]
	v_pk_mul_f32 v[156:157], v[156:157], s[34:35] op_sel_hi:[1,0]
	v_pk_mul_f32 v[6:7], v[150:151], s[4:5] op_sel_hi:[1,0]
	v_pk_mul_f32 v[8:9], v[152:153], s[4:5] op_sel_hi:[1,0]
	v_pk_mul_f32 v[20:21], v[154:155], s[4:5] op_sel_hi:[1,0]
	v_pk_mul_f32 v[22:23], v[156:157], s[4:5] op_sel_hi:[1,0]
	v_exp_f32_e32 v6, v6
	v_exp_f32_e32 v7, v7
	v_exp_f32_e32 v8, v8
	v_exp_f32_e32 v9, v9
	v_exp_f32_e32 v20, v20
	v_exp_f32_e32 v21, v21
	v_exp_f32_e32 v22, v22
	v_exp_f32_e32 v23, v23
	v_pk_add_f32 v[6:7], v[6:7], 1.0 op_sel_hi:[1,0]
	v_pk_add_f32 v[8:9], v[8:9], 1.0 op_sel_hi:[1,0]
	v_pk_add_f32 v[20:21], v[20:21], 1.0 op_sel_hi:[1,0]
	v_pk_add_f32 v[22:23], v[22:23], 1.0 op_sel_hi:[1,0]
	v_rcp_f32_e32 v6, v6
	v_rcp_f32_e32 v7, v7
	v_rcp_f32_e32 v8, v8
	v_rcp_f32_e32 v9, v9
	v_rcp_f32_e32 v20, v20
	v_rcp_f32_e32 v21, v21
	v_rcp_f32_e32 v22, v22
	v_rcp_f32_e32 v23, v23
	v_pk_mul_f32 v[150:151], v[150:151], v[6:7]
	v_pk_mul_f32 v[152:153], v[152:153], v[8:9]
	v_pk_mul_f32 v[154:155], v[154:155], v[20:21]
	v_pk_mul_f32 v[156:157], v[156:157], v[22:23]
	v_med3_f32 v150, v150, s35, v225
	v_med3_f32 v151, v151, s35, v225
	v_med3_f32 v152, v152, s35, v225
	v_med3_f32 v153, v153, s35, v225
	v_med3_f32 v154, v154, s35, v225
	v_med3_f32 v155, v155, s35, v225
	v_med3_f32 v156, v156, s35, v225
	v_med3_f32 v157, v157, s35, v225
	v_pk_mul_f32 v[158:159], v[158:159], s[34:35] op_sel_hi:[1,0]
	v_pk_mul_f32 v[160:161], v[160:161], s[34:35] op_sel_hi:[1,0]
	v_pk_mul_f32 v[162:163], v[162:163], s[34:35] op_sel_hi:[1,0]
	v_pk_mul_f32 v[164:165], v[164:165], s[34:35] op_sel_hi:[1,0]
	v_pk_mul_f32 v[6:7], v[158:159], s[4:5] op_sel_hi:[1,0]
	v_pk_mul_f32 v[8:9], v[160:161], s[4:5] op_sel_hi:[1,0]
	v_pk_mul_f32 v[20:21], v[162:163], s[4:5] op_sel_hi:[1,0]
	v_pk_mul_f32 v[22:23], v[164:165], s[4:5] op_sel_hi:[1,0]
	v_exp_f32_e32 v6, v6
	v_exp_f32_e32 v7, v7
	v_exp_f32_e32 v8, v8
	v_exp_f32_e32 v9, v9
	v_exp_f32_e32 v20, v20
	v_exp_f32_e32 v21, v21
	v_exp_f32_e32 v22, v22
	v_exp_f32_e32 v23, v23
	v_pk_add_f32 v[6:7], v[6:7], 1.0 op_sel_hi:[1,0]
	v_pk_add_f32 v[8:9], v[8:9], 1.0 op_sel_hi:[1,0]
	v_pk_add_f32 v[20:21], v[20:21], 1.0 op_sel_hi:[1,0]
	v_pk_add_f32 v[22:23], v[22:23], 1.0 op_sel_hi:[1,0]
	v_rcp_f32_e32 v6, v6
	v_rcp_f32_e32 v7, v7
	v_rcp_f32_e32 v8, v8
	v_rcp_f32_e32 v9, v9
	v_rcp_f32_e32 v20, v20
	v_rcp_f32_e32 v21, v21
	v_rcp_f32_e32 v22, v22
	v_rcp_f32_e32 v23, v23
	v_pk_mul_f32 v[158:159], v[158:159], v[6:7]
	v_pk_mul_f32 v[160:161], v[160:161], v[8:9]
	v_pk_mul_f32 v[162:163], v[162:163], v[20:21]
	v_pk_mul_f32 v[164:165], v[164:165], v[22:23]
	v_med3_f32 v158, v158, s35, v225
	v_med3_f32 v159, v159, s35, v225
	v_med3_f32 v160, v160, s35, v225
	v_med3_f32 v161, v161, s35, v225
	v_med3_f32 v162, v162, s35, v225
	v_med3_f32 v163, v163, s35, v225
	v_med3_f32 v164, v164, s35, v225
	v_med3_f32 v165, v165, s35, v225
	v_cvt_pk_fp8_f32 v158, v158, v159
	v_cvt_pk_fp8_f32 v159, v150, v151
	v_cvt_pk_fp8_f32 v158, v160, v161 op_sel:[0,0,1]
	v_cvt_pk_fp8_f32 v159, v152, v153 op_sel:[0,0,1]
	v_cvt_pk_fp8_f32 v160, v162, v163
	v_cvt_pk_fp8_f32 v161, v154, v155
	v_cvt_pk_fp8_f32 v160, v164, v165 op_sel:[0,0,1]
	v_cvt_pk_fp8_f32 v161, v156, v157 op_sel:[0,0,1]
	s_nop 1
	v_permlane16_swap_b32_e32 v158, v160
	v_permlane16_swap_b32_e32 v159, v161
	global_store_dwordx4 v[12:13], v[158:161], off
	v_pk_mul_f32 v[134:135], v[134:135], s[34:35] op_sel_hi:[1,0]
	v_pk_mul_f32 v[136:137], v[136:137], s[34:35] op_sel_hi:[1,0]
	v_pk_mul_f32 v[138:139], v[138:139], s[34:35] op_sel_hi:[1,0]
	v_pk_mul_f32 v[140:141], v[140:141], s[34:35] op_sel_hi:[1,0]
	v_pk_mul_f32 v[6:7], v[134:135], s[4:5] op_sel_hi:[1,0]
	v_pk_mul_f32 v[8:9], v[136:137], s[4:5] op_sel_hi:[1,0]
	v_pk_mul_f32 v[20:21], v[138:139], s[4:5] op_sel_hi:[1,0]
	v_pk_mul_f32 v[22:23], v[140:141], s[4:5] op_sel_hi:[1,0]
	v_exp_f32_e32 v6, v6
	v_exp_f32_e32 v7, v7
	v_exp_f32_e32 v8, v8
	v_exp_f32_e32 v9, v9
	v_exp_f32_e32 v20, v20
	v_exp_f32_e32 v21, v21
	v_exp_f32_e32 v22, v22
	v_exp_f32_e32 v23, v23
	v_pk_add_f32 v[6:7], v[6:7], 1.0 op_sel_hi:[1,0]
	v_pk_add_f32 v[8:9], v[8:9], 1.0 op_sel_hi:[1,0]
	v_pk_add_f32 v[20:21], v[20:21], 1.0 op_sel_hi:[1,0]
	v_pk_add_f32 v[22:23], v[22:23], 1.0 op_sel_hi:[1,0]
	v_rcp_f32_e32 v6, v6
	v_rcp_f32_e32 v7, v7
	v_rcp_f32_e32 v8, v8
	v_rcp_f32_e32 v9, v9
	v_rcp_f32_e32 v20, v20
	v_rcp_f32_e32 v21, v21
	v_rcp_f32_e32 v22, v22
	v_rcp_f32_e32 v23, v23
	v_pk_mul_f32 v[134:135], v[134:135], v[6:7]
	v_pk_mul_f32 v[136:137], v[136:137], v[8:9]
	v_pk_mul_f32 v[138:139], v[138:139], v[20:21]
	v_pk_mul_f32 v[140:141], v[140:141], v[22:23]
	v_med3_f32 v134, v134, s35, v225
	v_med3_f32 v135, v135, s35, v225
	v_med3_f32 v136, v136, s35, v225
	v_med3_f32 v137, v137, s35, v225
	v_med3_f32 v138, v138, s35, v225
; DI unsigned pk4_fp8(float a, float b, float c_, float d) { int w = 0; w = __builtin_amdgcn_cvt_pk_fp8_f32(clamp8(a), clamp8(b), w, false); w = __builtin_amdgcn_cvt_pk_fp8_f32(clamp8(c_), clamp8(d), w, true); return (unsigned)w; }
; DI float sigmoidf_(float x) { return __builtin_amdgcn_rcpf(1.0f + __builtin_amdgcn_exp2f(-x * LOG2E)); }
;     DI void operator()(const f32x4 (&acc)[2][2][4][2], const Unit& u, int wr, int wc, int fr, int fq) const {
;     ...
;             else if (pn < 12) {
; #pragma unroll
;                 for (int ai = 0; ai < 2; ++ai)
; #pragma unroll
;                     for (int m = 0; m < 4; ++m) { unsigned char* rowp = (unsigned char*)sr + (size_t)(row0 + ai * 128 + m * 16) * 1024 + (pn - 8) * 256 + wc * 32 + 8 * fq;
;                         u32x2 o[2];
; #pragma unroll
;                         for (int bj = 0; bj < 2; ++bj) { const f32x4 v0 = acc[ai][bj][m][0] * W8_INV, v1 = acc[ai][bj][m][1] * W8_INV;
;                             o[bj].x = pk4_fp8(v0[0] * sigmoidf_(v0[0]), v0[1] * sigmoidf_(v0[1]), v0[2] * sigmoidf_(v0[2]), v0[3] * sigmoidf_(v0[3]));
;                             o[bj].y = pk4_fp8(v1[0] * sigmoidf_(v1[0]), v1[1] * sigmoidf_(v1[1]), v1[2] * sigmoidf_(v1[2]), v1[3] * sigmoidf_(v1[3])); }
;                         st_pair16(rowp, 128, o[0], o[1], fq); }
;                 return; }
	v_med3_f32 v139, v139, s35, v225
	v_med3_f32 v140, v140, s35, v225
	v_med3_f32 v141, v141, s35, v225
	v_pk_mul_f32 v[142:143], v[142:143], s[34:35] op_sel_hi:[1,0]
	v_pk_mul_f32 v[144:145], v[144:145], s[34:35] op_sel_hi:[1,0]
	v_pk_mul_f32 v[146:147], v[146:147], s[34:35] op_sel_hi:[1,0]
	v_pk_mul_f32 v[148:149], v[148:149], s[34:35] op_sel_hi:[1,0]
	v_pk_mul_f32 v[6:7], v[142:143], s[4:5] op_sel_hi:[1,0]
	v_pk_mul_f32 v[8:9], v[144:145], s[4:5] op_sel_hi:[1,0]
	v_pk_mul_f32 v[20:21], v[146:147], s[4:5] op_sel_hi:[1,0]
	v_pk_mul_f32 v[22:23], v[148:149], s[4:5] op_sel_hi:[1,0]
	v_exp_f32_e32 v6, v6
	v_exp_f32_e32 v7, v7
	v_exp_f32_e32 v8, v8
	v_exp_f32_e32 v9, v9
	v_exp_f32_e32 v20, v20
	v_exp_f32_e32 v21, v21
	v_exp_f32_e32 v22, v22
	v_exp_f32_e32 v23, v23
	v_pk_add_f32 v[6:7], v[6:7], 1.0 op_sel_hi:[1,0]
	v_pk_add_f32 v[8:9], v[8:9], 1.0 op_sel_hi:[1,0]
	v_pk_add_f32 v[20:21], v[20:21], 1.0 op_sel_hi:[1,0]
	v_pk_add_f32 v[22:23], v[22:23], 1.0 op_sel_hi:[1,0]
	v_rcp_f32_e32 v6, v6
	v_rcp_f32_e32 v7, v7
	v_rcp_f32_e32 v8, v8
	v_rcp_f32_e32 v9, v9
	v_rcp_f32_e32 v20, v20
	v_rcp_f32_e32 v21, v21
	v_rcp_f32_e32 v22, v22
	v_rcp_f32_e32 v23, v23
	v_pk_mul_f32 v[142:143], v[142:143], v[6:7]
	v_pk_mul_f32 v[144:145], v[144:145], v[8:9]
	v_pk_mul_f32 v[146:147], v[146:147], v[20:21]
	v_pk_mul_f32 v[148:149], v[148:149], v[22:23]
	v_med3_f32 v142, v142, s35, v225
	v_med3_f32 v143, v143, s35, v225
	v_med3_f32 v144, v144, s35, v225
	v_med3_f32 v145, v145, s35, v225
	v_med3_f32 v146, v146, s35, v225
	v_med3_f32 v147, v147, s35, v225
	v_med3_f32 v148, v148, s35, v225
	v_med3_f32 v149, v149, s35, v225
	v_cvt_pk_fp8_f32 v142, v142, v143
	v_cvt_pk_fp8_f32 v143, v134, v135
	v_cvt_pk_fp8_f32 v142, v144, v145 op_sel:[0,0,1]
	v_cvt_pk_fp8_f32 v143, v136, v137 op_sel:[0,0,1]
	v_cvt_pk_fp8_f32 v144, v146, v147
	v_cvt_pk_fp8_f32 v145, v138, v139
	v_cvt_pk_fp8_f32 v144, v148, v149 op_sel:[0,0,1]
	v_cvt_pk_fp8_f32 v145, v140, v141 op_sel:[0,0,1]
	v_add_co_u32_e32 v14, vcc, 0x4000, v12
	s_nop 0
	v_permlane16_swap_b32_e32 v142, v144
	v_addc_co_u32_e32 v15, vcc, 0, v13, vcc
	v_permlane16_swap_b32_e32 v143, v145
	global_store_dwordx4 v[14:15], v[142:145], off
	v_pk_mul_f32 v[118:119], v[118:119], s[34:35] op_sel_hi:[1,0]
	v_pk_mul_f32 v[120:121], v[120:121], s[34:35] op_sel_hi:[1,0]
	v_pk_mul_f32 v[122:123], v[122:123], s[34:35] op_sel_hi:[1,0]
	v_pk_mul_f32 v[124:125], v[124:125], s[34:35] op_sel_hi:[1,0]
	v_pk_mul_f32 v[6:7], v[118:119], s[4:5] op_sel_hi:[1,0]
	v_pk_mul_f32 v[8:9], v[120:121], s[4:5] op_sel_hi:[1,0]
	v_pk_mul_f32 v[20:21], v[122:123], s[4:5] op_sel_hi:[1,0]
	v_pk_mul_f32 v[22:23], v[124:125], s[4:5] op_sel_hi:[1,0]
	v_exp_f32_e32 v6, v6
	v_exp_f32_e32 v7, v7
	v_exp_f32_e32 v8, v8
	v_exp_f32_e32 v9, v9
	v_exp_f32_e32 v20, v20
	v_exp_f32_e32 v21, v21
	v_exp_f32_e32 v22, v22
	v_exp_f32_e32 v23, v23
	v_pk_add_f32 v[6:7], v[6:7], 1.0 op_sel_hi:[1,0]
	v_pk_add_f32 v[8:9], v[8:9], 1.0 op_sel_hi:[1,0]
	v_pk_add_f32 v[20:21], v[20:21], 1.0 op_sel_hi:[1,0]
	v_pk_add_f32 v[22:23], v[22:23], 1.0 op_sel_hi:[1,0]
	v_rcp_f32_e32 v6, v6
	v_rcp_f32_e32 v7, v7
	v_rcp_f32_e32 v8, v8
	v_rcp_f32_e32 v9, v9
	v_rcp_f32_e32 v20, v20
	v_rcp_f32_e32 v21, v21
	v_rcp_f32_e32 v22, v22
	v_rcp_f32_e32 v23, v23
	v_pk_mul_f32 v[118:119], v[118:119], v[6:7]
	v_pk_mul_f32 v[120:121], v[120:121], v[8:9]
	v_pk_mul_f32 v[122:123], v[122:123], v[20:21]
	v_pk_mul_f32 v[124:125], v[124:125], v[22:23]
	v_med3_f32 v118, v118, s35, v225
	v_med3_f32 v119, v119, s35, v225
	v_med3_f32 v120, v120, s35, v225
	v_med3_f32 v121, v121, s35, v225
	v_med3_f32 v122, v122, s35, v225
	v_med3_f32 v123, v123, s35, v225
	v_med3_f32 v124, v124, s35, v225
	v_med3_f32 v125, v125, s35, v225
	v_pk_mul_f32 v[126:127], v[126:127], s[34:35] op_sel_hi:[1,0]
	v_pk_mul_f32 v[128:129], v[128:129], s[34:35] op_sel_hi:[1,0]
	v_pk_mul_f32 v[130:131], v[130:131], s[34:35] op_sel_hi:[1,0]
	v_pk_mul_f32 v[132:133], v[132:133], s[34:35] op_sel_hi:[1,0]
	v_pk_mul_f32 v[6:7], v[126:127], s[4:5] op_sel_hi:[1,0]
	v_pk_mul_f32 v[8:9], v[128:129], s[4:5] op_sel_hi:[1,0]
	v_pk_mul_f32 v[20:21], v[130:131], s[4:5] op_sel_hi:[1,0]
	v_pk_mul_f32 v[22:23], v[132:133], s[4:5] op_sel_hi:[1,0]
	v_exp_f32_e32 v6, v6
	v_exp_f32_e32 v7, v7
	v_exp_f32_e32 v8, v8
	v_exp_f32_e32 v9, v9
	v_exp_f32_e32 v20, v20
	v_exp_f32_e32 v21, v21
	v_exp_f32_e32 v22, v22
	v_exp_f32_e32 v23, v23
	v_pk_add_f32 v[6:7], v[6:7], 1.0 op_sel_hi:[1,0]
	v_pk_add_f32 v[8:9], v[8:9], 1.0 op_sel_hi:[1,0]
	v_pk_add_f32 v[20:21], v[20:21], 1.0 op_sel_hi:[1,0]
	v_pk_add_f32 v[22:23], v[22:23], 1.0 op_sel_hi:[1,0]
	v_rcp_f32_e32 v6, v6
	v_rcp_f32_e32 v7, v7
	v_rcp_f32_e32 v8, v8
	v_rcp_f32_e32 v9, v9
	v_rcp_f32_e32 v20, v20
	v_rcp_f32_e32 v21, v21
	v_rcp_f32_e32 v22, v22
	v_rcp_f32_e32 v23, v23
	v_pk_mul_f32 v[126:127], v[126:127], v[6:7]
	v_pk_mul_f32 v[128:129], v[128:129], v[8:9]
	v_pk_mul_f32 v[130:131], v[130:131], v[20:21]
	v_pk_mul_f32 v[132:133], v[132:133], v[22:23]
	v_med3_f32 v126, v126, s35, v225
	v_med3_f32 v127, v127, s35, v225
	v_med3_f32 v128, v128, s35, v225
	v_med3_f32 v129, v129, s35, v225
	v_med3_f32 v130, v130, s35, v225
	v_med3_f32 v131, v131, s35, v225
	v_med3_f32 v132, v132, s35, v225
	v_med3_f32 v133, v133, s35, v225
	v_cvt_pk_fp8_f32 v126, v126, v127
	v_cvt_pk_fp8_f32 v127, v118, v119
	v_cvt_pk_fp8_f32 v126, v128, v129 op_sel:[0,0,1]
	v_cvt_pk_fp8_f32 v127, v120, v121 op_sel:[0,0,1]
	v_cvt_pk_fp8_f32 v128, v130, v131
	v_cvt_pk_fp8_f32 v129, v122, v123
	v_cvt_pk_fp8_f32 v128, v132, v133 op_sel:[0,0,1]
	v_cvt_pk_fp8_f32 v129, v124, v125 op_sel:[0,0,1]
	v_add_co_u32_e32 v14, vcc, 0x8000, v12
	s_nop 0
	v_permlane16_swap_b32_e32 v126, v128
; DI unsigned pk4_fp8(float a, float b, float c_, float d) { int w = 0; w = __builtin_amdgcn_cvt_pk_fp8_f32(clamp8(a), clamp8(b), w, false); w = __builtin_amdgcn_cvt_pk_fp8_f32(clamp8(c_), clamp8(d), w, true); return (unsigned)w; }
; DI float sigmoidf_(float x) { return __builtin_amdgcn_rcpf(1.0f + __builtin_amdgcn_exp2f(-x * LOG2E)); }
;     DI void operator()(const f32x4 (&acc)[2][2][4][2], const Unit& u, int wr, int wc, int fr, int fq) const {
;     ...
;             else if (pn < 12) {
; #pragma unroll
;                 for (int ai = 0; ai < 2; ++ai)
; #pragma unroll
;                     for (int m = 0; m < 4; ++m) { unsigned char* rowp = (unsigned char*)sr + (size_t)(row0 + ai * 128 + m * 16) * 1024 + (pn - 8) * 256 + wc * 32 + 8 * fq;
;                         u32x2 o[2];
; #pragma unroll
;                         for (int bj = 0; bj < 2; ++bj) { const f32x4 v0 = acc[ai][bj][m][0] * W8_INV, v1 = acc[ai][bj][m][1] * W8_INV;
;                             o[bj].x = pk4_fp8(v0[0] * sigmoidf_(v0[0]), v0[1] * sigmoidf_(v0[1]), v0[2] * sigmoidf_(v0[2]), v0[3] * sigmoidf_(v0[3]));
;                             o[bj].y = pk4_fp8(v1[0] * sigmoidf_(v1[0]), v1[1] * sigmoidf_(v1[1]), v1[2] * sigmoidf_(v1[2]), v1[3] * sigmoidf_(v1[3])); }
;                         st_pair16(rowp, 128, o[0], o[1], fq); }
;                 return; }
	v_addc_co_u32_e32 v15, vcc, 0, v13, vcc
	v_permlane16_swap_b32_e32 v127, v129
	global_store_dwordx4 v[14:15], v[126:129], off
	v_pk_mul_f32 v[102:103], v[102:103], s[34:35] op_sel_hi:[1,0]
	v_pk_mul_f32 v[104:105], v[104:105], s[34:35] op_sel_hi:[1,0]
	v_pk_mul_f32 v[106:107], v[106:107], s[34:35] op_sel_hi:[1,0]
	v_pk_mul_f32 v[108:109], v[108:109], s[34:35] op_sel_hi:[1,0]
	v_pk_mul_f32 v[6:7], v[102:103], s[4:5] op_sel_hi:[1,0]
	v_pk_mul_f32 v[8:9], v[104:105], s[4:5] op_sel_hi:[1,0]
	v_pk_mul_f32 v[20:21], v[106:107], s[4:5] op_sel_hi:[1,0]
	v_pk_mul_f32 v[22:23], v[108:109], s[4:5] op_sel_hi:[1,0]
	v_exp_f32_e32 v6, v6
	v_exp_f32_e32 v7, v7
	v_exp_f32_e32 v8, v8
	v_exp_f32_e32 v9, v9
	v_exp_f32_e32 v20, v20
	v_exp_f32_e32 v21, v21
	v_exp_f32_e32 v22, v22
	v_exp_f32_e32 v23, v23
	v_pk_add_f32 v[6:7], v[6:7], 1.0 op_sel_hi:[1,0]
	v_pk_add_f32 v[8:9], v[8:9], 1.0 op_sel_hi:[1,0]
	v_pk_add_f32 v[20:21], v[20:21], 1.0 op_sel_hi:[1,0]
	v_pk_add_f32 v[22:23], v[22:23], 1.0 op_sel_hi:[1,0]
	v_rcp_f32_e32 v6, v6
	v_rcp_f32_e32 v7, v7
	v_rcp_f32_e32 v8, v8
	v_rcp_f32_e32 v9, v9
	v_rcp_f32_e32 v20, v20
	v_rcp_f32_e32 v21, v21
	v_rcp_f32_e32 v22, v22
	v_rcp_f32_e32 v23, v23
	v_pk_mul_f32 v[102:103], v[102:103], v[6:7]
	v_pk_mul_f32 v[104:105], v[104:105], v[8:9]
	v_pk_mul_f32 v[106:107], v[106:107], v[20:21]
	v_pk_mul_f32 v[108:109], v[108:109], v[22:23]
	v_med3_f32 v102, v102, s35, v225
	v_med3_f32 v103, v103, s35, v225
	v_med3_f32 v104, v104, s35, v225
	v_med3_f32 v105, v105, s35, v225
	v_med3_f32 v106, v106, s35, v225
	v_med3_f32 v107, v107, s35, v225
	v_med3_f32 v108, v108, s35, v225
	v_med3_f32 v109, v109, s35, v225
	v_pk_mul_f32 v[110:111], v[110:111], s[34:35] op_sel_hi:[1,0]
	v_pk_mul_f32 v[112:113], v[112:113], s[34:35] op_sel_hi:[1,0]
	v_pk_mul_f32 v[114:115], v[114:115], s[34:35] op_sel_hi:[1,0]
	v_pk_mul_f32 v[116:117], v[116:117], s[34:35] op_sel_hi:[1,0]
	v_pk_mul_f32 v[6:7], v[110:111], s[4:5] op_sel_hi:[1,0]
	v_pk_mul_f32 v[8:9], v[112:113], s[4:5] op_sel_hi:[1,0]
	v_pk_mul_f32 v[20:21], v[114:115], s[4:5] op_sel_hi:[1,0]
	v_pk_mul_f32 v[22:23], v[116:117], s[4:5] op_sel_hi:[1,0]
	v_exp_f32_e32 v6, v6
	v_exp_f32_e32 v7, v7
	v_exp_f32_e32 v8, v8
	v_exp_f32_e32 v9, v9
	v_exp_f32_e32 v20, v20
	v_exp_f32_e32 v21, v21
	v_exp_f32_e32 v22, v22
	v_exp_f32_e32 v23, v23
	v_pk_add_f32 v[6:7], v[6:7], 1.0 op_sel_hi:[1,0]
	v_pk_add_f32 v[8:9], v[8:9], 1.0 op_sel_hi:[1,0]
	v_pk_add_f32 v[20:21], v[20:21], 1.0 op_sel_hi:[1,0]
	v_pk_add_f32 v[22:23], v[22:23], 1.0 op_sel_hi:[1,0]
	v_rcp_f32_e32 v6, v6
	v_rcp_f32_e32 v7, v7
	v_rcp_f32_e32 v8, v8
	v_rcp_f32_e32 v9, v9
	v_rcp_f32_e32 v20, v20
	v_rcp_f32_e32 v21, v21
	v_rcp_f32_e32 v22, v22
	v_rcp_f32_e32 v23, v23
	v_pk_mul_f32 v[110:111], v[110:111], v[6:7]
	v_pk_mul_f32 v[112:113], v[112:113], v[8:9]
	v_pk_mul_f32 v[114:115], v[114:115], v[20:21]
	v_pk_mul_f32 v[116:117], v[116:117], v[22:23]
	v_med3_f32 v110, v110, s35, v225
	v_med3_f32 v111, v111, s35, v225
	v_med3_f32 v112, v112, s35, v225
	v_med3_f32 v113, v113, s35, v225
	v_med3_f32 v114, v114, s35, v225
	v_med3_f32 v115, v115, s35, v225
	v_med3_f32 v116, v116, s35, v225
	v_med3_f32 v117, v117, s35, v225
	v_cvt_pk_fp8_f32 v110, v110, v111
	v_cvt_pk_fp8_f32 v111, v102, v103
	v_cvt_pk_fp8_f32 v110, v112, v113 op_sel:[0,0,1]
	v_cvt_pk_fp8_f32 v111, v104, v105 op_sel:[0,0,1]
	v_cvt_pk_fp8_f32 v112, v114, v115
	v_cvt_pk_fp8_f32 v113, v106, v107
	v_cvt_pk_fp8_f32 v112, v116, v117 op_sel:[0,0,1]
	v_cvt_pk_fp8_f32 v113, v108, v109 op_sel:[0,0,1]
	v_add_co_u32_e32 v14, vcc, 0xc000, v12
	s_nop 0
	v_permlane16_swap_b32_e32 v110, v112
	v_addc_co_u32_e32 v15, vcc, 0, v13, vcc
	v_permlane16_swap_b32_e32 v111, v113
	global_store_dwordx4 v[14:15], v[110:113], off
	v_pk_mul_f32 v[86:87], v[86:87], s[34:35] op_sel_hi:[1,0]
	v_pk_mul_f32 v[88:89], v[88:89], s[34:35] op_sel_hi:[1,0]
	v_pk_mul_f32 v[90:91], v[90:91], s[34:35] op_sel_hi:[1,0]
	v_pk_mul_f32 v[92:93], v[92:93], s[34:35] op_sel_hi:[1,0]
	v_pk_mul_f32 v[6:7], v[86:87], s[4:5] op_sel_hi:[1,0]
	v_pk_mul_f32 v[8:9], v[88:89], s[4:5] op_sel_hi:[1,0]
	v_pk_mul_f32 v[20:21], v[90:91], s[4:5] op_sel_hi:[1,0]
	v_pk_mul_f32 v[22:23], v[92:93], s[4:5] op_sel_hi:[1,0]
	v_exp_f32_e32 v6, v6
	v_exp_f32_e32 v7, v7
	v_exp_f32_e32 v8, v8
	v_exp_f32_e32 v9, v9
	v_exp_f32_e32 v20, v20
	v_exp_f32_e32 v21, v21
	v_exp_f32_e32 v22, v22
	v_exp_f32_e32 v23, v23
	v_pk_add_f32 v[6:7], v[6:7], 1.0 op_sel_hi:[1,0]
	v_pk_add_f32 v[8:9], v[8:9], 1.0 op_sel_hi:[1,0]
	v_pk_add_f32 v[20:21], v[20:21], 1.0 op_sel_hi:[1,0]
	v_pk_add_f32 v[22:23], v[22:23], 1.0 op_sel_hi:[1,0]
	v_rcp_f32_e32 v6, v6
	v_rcp_f32_e32 v7, v7
	v_rcp_f32_e32 v8, v8
	v_rcp_f32_e32 v9, v9
	v_rcp_f32_e32 v20, v20
	v_rcp_f32_e32 v21, v21
	v_rcp_f32_e32 v22, v22
	v_rcp_f32_e32 v23, v23
	v_pk_mul_f32 v[86:87], v[86:87], v[6:7]
	v_pk_mul_f32 v[88:89], v[88:89], v[8:9]
	v_pk_mul_f32 v[90:91], v[90:91], v[20:21]
	v_pk_mul_f32 v[92:93], v[92:93], v[22:23]
	v_med3_f32 v86, v86, s35, v225
	v_med3_f32 v87, v87, s35, v225
	v_med3_f32 v88, v88, s35, v225
	v_med3_f32 v89, v89, s35, v225
	v_med3_f32 v90, v90, s35, v225
	v_med3_f32 v91, v91, s35, v225
	v_med3_f32 v92, v92, s35, v225
	v_med3_f32 v93, v93, s35, v225
	v_pk_mul_f32 v[94:95], v[94:95], s[34:35] op_sel_hi:[1,0]
	v_pk_mul_f32 v[96:97], v[96:97], s[34:35] op_sel_hi:[1,0]
	v_pk_mul_f32 v[98:99], v[98:99], s[34:35] op_sel_hi:[1,0]
	v_pk_mul_f32 v[100:101], v[100:101], s[34:35] op_sel_hi:[1,0]
	v_pk_mul_f32 v[6:7], v[94:95], s[4:5] op_sel_hi:[1,0]
	v_pk_mul_f32 v[8:9], v[96:97], s[4:5] op_sel_hi:[1,0]
	v_pk_mul_f32 v[20:21], v[98:99], s[4:5] op_sel_hi:[1,0]
	v_pk_mul_f32 v[22:23], v[100:101], s[4:5] op_sel_hi:[1,0]
; DI unsigned pk4_fp8(float a, float b, float c_, float d) { int w = 0; w = __builtin_amdgcn_cvt_pk_fp8_f32(clamp8(a), clamp8(b), w, false); w = __builtin_amdgcn_cvt_pk_fp8_f32(clamp8(c_), clamp8(d), w, true); return (unsigned)w; }
; DI float sigmoidf_(float x) { return __builtin_amdgcn_rcpf(1.0f + __builtin_amdgcn_exp2f(-x * LOG2E)); }
;     DI void operator()(const f32x4 (&acc)[2][2][4][2], const Unit& u, int wr, int wc, int fr, int fq) const {
;     ...
;             else if (pn < 12) {
; #pragma unroll
;                 for (int ai = 0; ai < 2; ++ai)
; #pragma unroll
;                     for (int m = 0; m < 4; ++m) { unsigned char* rowp = (unsigned char*)sr + (size_t)(row0 + ai * 128 + m * 16) * 1024 + (pn - 8) * 256 + wc * 32 + 8 * fq;
;                         u32x2 o[2];
; #pragma unroll
;                         for (int bj = 0; bj < 2; ++bj) { const f32x4 v0 = acc[ai][bj][m][0] * W8_INV, v1 = acc[ai][bj][m][1] * W8_INV;
;                             o[bj].x = pk4_fp8(v0[0] * sigmoidf_(v0[0]), v0[1] * sigmoidf_(v0[1]), v0[2] * sigmoidf_(v0[2]), v0[3] * sigmoidf_(v0[3]));
;                             o[bj].y = pk4_fp8(v1[0] * sigmoidf_(v1[0]), v1[1] * sigmoidf_(v1[1]), v1[2] * sigmoidf_(v1[2]), v1[3] * sigmoidf_(v1[3])); }
;                         st_pair16(rowp, 128, o[0], o[1], fq); }
;                 return; }
	v_exp_f32_e32 v6, v6
	v_exp_f32_e32 v7, v7
	v_exp_f32_e32 v8, v8
	v_exp_f32_e32 v9, v9
	v_exp_f32_e32 v20, v20
	v_exp_f32_e32 v21, v21
	v_exp_f32_e32 v22, v22
	v_exp_f32_e32 v23, v23
	v_pk_add_f32 v[6:7], v[6:7], 1.0 op_sel_hi:[1,0]
	v_pk_add_f32 v[8:9], v[8:9], 1.0 op_sel_hi:[1,0]
	v_pk_add_f32 v[20:21], v[20:21], 1.0 op_sel_hi:[1,0]
	v_pk_add_f32 v[22:23], v[22:23], 1.0 op_sel_hi:[1,0]
	v_rcp_f32_e32 v6, v6
	v_rcp_f32_e32 v7, v7
	v_rcp_f32_e32 v8, v8
	v_rcp_f32_e32 v9, v9
	v_rcp_f32_e32 v20, v20
	v_rcp_f32_e32 v21, v21
	v_rcp_f32_e32 v22, v22
	v_rcp_f32_e32 v23, v23
	v_pk_mul_f32 v[94:95], v[94:95], v[6:7]
	v_pk_mul_f32 v[96:97], v[96:97], v[8:9]
	v_pk_mul_f32 v[98:99], v[98:99], v[20:21]
	v_pk_mul_f32 v[100:101], v[100:101], v[22:23]
	v_med3_f32 v94, v94, s35, v225
	v_med3_f32 v95, v95, s35, v225
	v_med3_f32 v96, v96, s35, v225
	v_med3_f32 v97, v97, s35, v225
	v_med3_f32 v98, v98, s35, v225
	v_med3_f32 v99, v99, s35, v225
	v_med3_f32 v100, v100, s35, v225
	v_med3_f32 v101, v101, s35, v225
	v_cvt_pk_fp8_f32 v94, v94, v95
	v_cvt_pk_fp8_f32 v95, v86, v87
	v_cvt_pk_fp8_f32 v94, v96, v97 op_sel:[0,0,1]
	v_cvt_pk_fp8_f32 v95, v88, v89 op_sel:[0,0,1]
	v_cvt_pk_fp8_f32 v96, v98, v99
	v_cvt_pk_fp8_f32 v97, v90, v91
	v_cvt_pk_fp8_f32 v96, v100, v101 op_sel:[0,0,1]
	v_cvt_pk_fp8_f32 v97, v92, v93 op_sel:[0,0,1]
	v_add_co_u32_e32 v14, vcc, 0x20000, v12
	s_nop 0
	v_permlane16_swap_b32_e32 v94, v96
	v_addc_co_u32_e32 v15, vcc, 0, v13, vcc
	v_permlane16_swap_b32_e32 v95, v97
	global_store_dwordx4 v[14:15], v[94:97], off
	v_pk_mul_f32 v[70:71], v[70:71], s[34:35] op_sel_hi:[1,0]
	v_pk_mul_f32 v[72:73], v[72:73], s[34:35] op_sel_hi:[1,0]
	v_pk_mul_f32 v[74:75], v[74:75], s[34:35] op_sel_hi:[1,0]
	v_pk_mul_f32 v[76:77], v[76:77], s[34:35] op_sel_hi:[1,0]
	v_pk_mul_f32 v[6:7], v[70:71], s[4:5] op_sel_hi:[1,0]
	v_pk_mul_f32 v[8:9], v[72:73], s[4:5] op_sel_hi:[1,0]
	v_pk_mul_f32 v[20:21], v[74:75], s[4:5] op_sel_hi:[1,0]
	v_pk_mul_f32 v[22:23], v[76:77], s[4:5] op_sel_hi:[1,0]
	v_exp_f32_e32 v6, v6
	v_exp_f32_e32 v7, v7
	v_exp_f32_e32 v8, v8
	v_exp_f32_e32 v9, v9
	v_exp_f32_e32 v20, v20
	v_exp_f32_e32 v21, v21
	v_exp_f32_e32 v22, v22
	v_exp_f32_e32 v23, v23
	v_pk_add_f32 v[6:7], v[6:7], 1.0 op_sel_hi:[1,0]
	v_pk_add_f32 v[8:9], v[8:9], 1.0 op_sel_hi:[1,0]
	v_pk_add_f32 v[20:21], v[20:21], 1.0 op_sel_hi:[1,0]
	v_pk_add_f32 v[22:23], v[22:23], 1.0 op_sel_hi:[1,0]
	v_rcp_f32_e32 v6, v6
	v_rcp_f32_e32 v7, v7
	v_rcp_f32_e32 v8, v8
	v_rcp_f32_e32 v9, v9
	v_rcp_f32_e32 v20, v20
	v_rcp_f32_e32 v21, v21
	v_rcp_f32_e32 v22, v22
	v_rcp_f32_e32 v23, v23
	v_pk_mul_f32 v[70:71], v[70:71], v[6:7]
	v_pk_mul_f32 v[72:73], v[72:73], v[8:9]
	v_pk_mul_f32 v[74:75], v[74:75], v[20:21]
	v_pk_mul_f32 v[76:77], v[76:77], v[22:23]
	v_med3_f32 v70, v70, s35, v225
	v_med3_f32 v71, v71, s35, v225
	v_med3_f32 v72, v72, s35, v225
	v_med3_f32 v73, v73, s35, v225
	v_med3_f32 v74, v74, s35, v225
	v_med3_f32 v75, v75, s35, v225
	v_med3_f32 v76, v76, s35, v225
	v_med3_f32 v77, v77, s35, v225
	v_pk_mul_f32 v[78:79], v[78:79], s[34:35] op_sel_hi:[1,0]
	v_pk_mul_f32 v[80:81], v[80:81], s[34:35] op_sel_hi:[1,0]
	v_pk_mul_f32 v[82:83], v[82:83], s[34:35] op_sel_hi:[1,0]
	v_pk_mul_f32 v[84:85], v[84:85], s[34:35] op_sel_hi:[1,0]
	v_pk_mul_f32 v[6:7], v[78:79], s[4:5] op_sel_hi:[1,0]
	v_pk_mul_f32 v[8:9], v[80:81], s[4:5] op_sel_hi:[1,0]
	v_pk_mul_f32 v[20:21], v[82:83], s[4:5] op_sel_hi:[1,0]
	v_pk_mul_f32 v[22:23], v[84:85], s[4:5] op_sel_hi:[1,0]
	v_exp_f32_e32 v6, v6
	v_exp_f32_e32 v7, v7
	v_exp_f32_e32 v8, v8
	v_exp_f32_e32 v9, v9
	v_exp_f32_e32 v20, v20
	v_exp_f32_e32 v21, v21
	v_exp_f32_e32 v22, v22
	v_exp_f32_e32 v23, v23
	v_pk_add_f32 v[6:7], v[6:7], 1.0 op_sel_hi:[1,0]
	v_pk_add_f32 v[8:9], v[8:9], 1.0 op_sel_hi:[1,0]
	v_pk_add_f32 v[20:21], v[20:21], 1.0 op_sel_hi:[1,0]
	v_pk_add_f32 v[22:23], v[22:23], 1.0 op_sel_hi:[1,0]
	v_rcp_f32_e32 v6, v6
	v_rcp_f32_e32 v7, v7
	v_rcp_f32_e32 v8, v8
	v_rcp_f32_e32 v9, v9
	v_rcp_f32_e32 v20, v20
	v_rcp_f32_e32 v21, v21
	v_rcp_f32_e32 v22, v22
	v_rcp_f32_e32 v23, v23
	v_pk_mul_f32 v[78:79], v[78:79], v[6:7]
	v_pk_mul_f32 v[80:81], v[80:81], v[8:9]
	v_pk_mul_f32 v[82:83], v[82:83], v[20:21]
	v_pk_mul_f32 v[84:85], v[84:85], v[22:23]
	v_med3_f32 v78, v78, s35, v225
	v_med3_f32 v79, v79, s35, v225
	v_med3_f32 v80, v80, s35, v225
	v_med3_f32 v81, v81, s35, v225
	v_med3_f32 v82, v82, s35, v225
	v_med3_f32 v83, v83, s35, v225
	v_med3_f32 v84, v84, s35, v225
	v_med3_f32 v85, v85, s35, v225
	v_cvt_pk_fp8_f32 v78, v78, v79
	v_cvt_pk_fp8_f32 v79, v70, v71
	v_cvt_pk_fp8_f32 v78, v80, v81 op_sel:[0,0,1]
	v_cvt_pk_fp8_f32 v79, v72, v73 op_sel:[0,0,1]
	v_cvt_pk_fp8_f32 v80, v82, v83
	v_cvt_pk_fp8_f32 v81, v74, v75
	v_cvt_pk_fp8_f32 v80, v84, v85 op_sel:[0,0,1]
	v_cvt_pk_fp8_f32 v81, v76, v77 op_sel:[0,0,1]
	v_add_co_u32_e32 v14, vcc, 0x24000, v12
	s_nop 0
	v_permlane16_swap_b32_e32 v78, v80
	v_addc_co_u32_e32 v15, vcc, 0, v13, vcc
	v_permlane16_swap_b32_e32 v79, v81
	global_store_dwordx4 v[14:15], v[78:81], off
	v_pk_mul_f32 v[54:55], v[54:55], s[34:35] op_sel_hi:[1,0]
	v_pk_mul_f32 v[56:57], v[56:57], s[34:35] op_sel_hi:[1,0]
	v_pk_mul_f32 v[58:59], v[58:59], s[34:35] op_sel_hi:[1,0]
	v_pk_mul_f32 v[60:61], v[60:61], s[34:35] op_sel_hi:[1,0]
	v_pk_mul_f32 v[6:7], v[54:55], s[4:5] op_sel_hi:[1,0]
	v_pk_mul_f32 v[8:9], v[56:57], s[4:5] op_sel_hi:[1,0]
	v_pk_mul_f32 v[20:21], v[58:59], s[4:5] op_sel_hi:[1,0]
	v_pk_mul_f32 v[22:23], v[60:61], s[4:5] op_sel_hi:[1,0]
	v_exp_f32_e32 v6, v6
	v_exp_f32_e32 v7, v7
	v_exp_f32_e32 v8, v8
	v_exp_f32_e32 v9, v9
	v_exp_f32_e32 v20, v20
	v_exp_f32_e32 v21, v21
	v_exp_f32_e32 v22, v22
	v_exp_f32_e32 v23, v23
; DI unsigned pk4_fp8(float a, float b, float c_, float d) { int w = 0; w = __builtin_amdgcn_cvt_pk_fp8_f32(clamp8(a), clamp8(b), w, false); w = __builtin_amdgcn_cvt_pk_fp8_f32(clamp8(c_), clamp8(d), w, true); return (unsigned)w; }
; DI float sigmoidf_(float x) { return __builtin_amdgcn_rcpf(1.0f + __builtin_amdgcn_exp2f(-x * LOG2E)); }
;     DI void operator()(const f32x4 (&acc)[2][2][4][2], const Unit& u, int wr, int wc, int fr, int fq) const {
;     ...
;             else if (pn < 12) {
; #pragma unroll
;                 for (int ai = 0; ai < 2; ++ai)
; #pragma unroll
;                     for (int m = 0; m < 4; ++m) { unsigned char* rowp = (unsigned char*)sr + (size_t)(row0 + ai * 128 + m * 16) * 1024 + (pn - 8) * 256 + wc * 32 + 8 * fq;
;                         u32x2 o[2];
; #pragma unroll
;                         for (int bj = 0; bj < 2; ++bj) { const f32x4 v0 = acc[ai][bj][m][0] * W8_INV, v1 = acc[ai][bj][m][1] * W8_INV;
;                             o[bj].x = pk4_fp8(v0[0] * sigmoidf_(v0[0]), v0[1] * sigmoidf_(v0[1]), v0[2] * sigmoidf_(v0[2]), v0[3] * sigmoidf_(v0[3]));
;                             o[bj].y = pk4_fp8(v1[0] * sigmoidf_(v1[0]), v1[1] * sigmoidf_(v1[1]), v1[2] * sigmoidf_(v1[2]), v1[3] * sigmoidf_(v1[3])); }
;                         st_pair16(rowp, 128, o[0], o[1], fq); }
;                 return; }
	v_pk_add_f32 v[6:7], v[6:7], 1.0 op_sel_hi:[1,0]
	v_pk_add_f32 v[8:9], v[8:9], 1.0 op_sel_hi:[1,0]
	v_pk_add_f32 v[20:21], v[20:21], 1.0 op_sel_hi:[1,0]
	v_pk_add_f32 v[22:23], v[22:23], 1.0 op_sel_hi:[1,0]
	v_rcp_f32_e32 v6, v6
	v_rcp_f32_e32 v7, v7
	v_rcp_f32_e32 v8, v8
	v_rcp_f32_e32 v9, v9
	v_rcp_f32_e32 v20, v20
	v_rcp_f32_e32 v21, v21
	v_rcp_f32_e32 v22, v22
	v_rcp_f32_e32 v23, v23
	v_pk_mul_f32 v[54:55], v[54:55], v[6:7]
	v_pk_mul_f32 v[56:57], v[56:57], v[8:9]
	v_pk_mul_f32 v[58:59], v[58:59], v[20:21]
	v_pk_mul_f32 v[60:61], v[60:61], v[22:23]
	v_med3_f32 v54, v54, s35, v225
	v_med3_f32 v55, v55, s35, v225
	v_med3_f32 v56, v56, s35, v225
	v_med3_f32 v57, v57, s35, v225
	v_med3_f32 v58, v58, s35, v225
	v_med3_f32 v59, v59, s35, v225
	v_med3_f32 v60, v60, s35, v225
	v_med3_f32 v61, v61, s35, v225
	v_pk_mul_f32 v[62:63], v[62:63], s[34:35] op_sel_hi:[1,0]
	v_pk_mul_f32 v[64:65], v[64:65], s[34:35] op_sel_hi:[1,0]
	v_pk_mul_f32 v[66:67], v[66:67], s[34:35] op_sel_hi:[1,0]
	v_pk_mul_f32 v[68:69], v[68:69], s[34:35] op_sel_hi:[1,0]
	v_pk_mul_f32 v[6:7], v[62:63], s[4:5] op_sel_hi:[1,0]
	v_pk_mul_f32 v[8:9], v[64:65], s[4:5] op_sel_hi:[1,0]
	v_pk_mul_f32 v[20:21], v[66:67], s[4:5] op_sel_hi:[1,0]
	v_pk_mul_f32 v[22:23], v[68:69], s[4:5] op_sel_hi:[1,0]
	v_exp_f32_e32 v6, v6
	v_exp_f32_e32 v7, v7
	v_exp_f32_e32 v8, v8
	v_exp_f32_e32 v9, v9
	v_exp_f32_e32 v20, v20
	v_exp_f32_e32 v21, v21
	v_exp_f32_e32 v22, v22
	v_exp_f32_e32 v23, v23
	v_pk_add_f32 v[6:7], v[6:7], 1.0 op_sel_hi:[1,0]
	v_pk_add_f32 v[8:9], v[8:9], 1.0 op_sel_hi:[1,0]
	v_pk_add_f32 v[20:21], v[20:21], 1.0 op_sel_hi:[1,0]
	v_pk_add_f32 v[22:23], v[22:23], 1.0 op_sel_hi:[1,0]
	v_rcp_f32_e32 v6, v6
	v_rcp_f32_e32 v7, v7
	v_rcp_f32_e32 v8, v8
	v_rcp_f32_e32 v9, v9
	v_rcp_f32_e32 v20, v20
	v_rcp_f32_e32 v21, v21
	v_rcp_f32_e32 v22, v22
	v_rcp_f32_e32 v23, v23
	v_pk_mul_f32 v[62:63], v[62:63], v[6:7]
	v_pk_mul_f32 v[64:65], v[64:65], v[8:9]
	v_pk_mul_f32 v[66:67], v[66:67], v[20:21]
	v_pk_mul_f32 v[68:69], v[68:69], v[22:23]
	v_med3_f32 v62, v62, s35, v225
	v_med3_f32 v63, v63, s35, v225
	v_med3_f32 v64, v64, s35, v225
	v_med3_f32 v65, v65, s35, v225
	v_med3_f32 v66, v66, s35, v225
	v_med3_f32 v67, v67, s35, v225
	v_med3_f32 v68, v68, s35, v225
	v_med3_f32 v69, v69, s35, v225
	v_cvt_pk_fp8_f32 v62, v62, v63
	v_cvt_pk_fp8_f32 v63, v54, v55
	v_cvt_pk_fp8_f32 v62, v64, v65 op_sel:[0,0,1]
	v_cvt_pk_fp8_f32 v63, v56, v57 op_sel:[0,0,1]
	v_cvt_pk_fp8_f32 v64, v66, v67
	v_cvt_pk_fp8_f32 v65, v58, v59
	v_cvt_pk_fp8_f32 v64, v68, v69 op_sel:[0,0,1]
	v_cvt_pk_fp8_f32 v65, v60, v61 op_sel:[0,0,1]
	v_add_co_u32_e32 v14, vcc, 0x28000, v12
	s_nop 0
	v_permlane16_swap_b32_e32 v62, v64
	v_addc_co_u32_e32 v15, vcc, 0, v13, vcc
	v_permlane16_swap_b32_e32 v63, v65
	global_store_dwordx4 v[14:15], v[62:65], off
	v_pk_mul_f32 v[38:39], v[38:39], s[34:35] op_sel_hi:[1,0]
	v_pk_mul_f32 v[40:41], v[40:41], s[34:35] op_sel_hi:[1,0]
	v_pk_mul_f32 v[42:43], v[42:43], s[34:35] op_sel_hi:[1,0]
	v_pk_mul_f32 v[44:45], v[44:45], s[34:35] op_sel_hi:[1,0]
	v_pk_mul_f32 v[6:7], v[38:39], s[4:5] op_sel_hi:[1,0]
	v_pk_mul_f32 v[8:9], v[40:41], s[4:5] op_sel_hi:[1,0]
	v_pk_mul_f32 v[20:21], v[42:43], s[4:5] op_sel_hi:[1,0]
	v_pk_mul_f32 v[22:23], v[44:45], s[4:5] op_sel_hi:[1,0]
	v_exp_f32_e32 v6, v6
	v_exp_f32_e32 v7, v7
	v_exp_f32_e32 v8, v8
	v_exp_f32_e32 v9, v9
	v_exp_f32_e32 v20, v20
	v_exp_f32_e32 v21, v21
	v_exp_f32_e32 v22, v22
	v_exp_f32_e32 v23, v23
	v_pk_add_f32 v[6:7], v[6:7], 1.0 op_sel_hi:[1,0]
	v_pk_add_f32 v[8:9], v[8:9], 1.0 op_sel_hi:[1,0]
	v_pk_add_f32 v[20:21], v[20:21], 1.0 op_sel_hi:[1,0]
	v_pk_add_f32 v[22:23], v[22:23], 1.0 op_sel_hi:[1,0]
	v_rcp_f32_e32 v6, v6
	v_rcp_f32_e32 v7, v7
	v_rcp_f32_e32 v8, v8
	v_rcp_f32_e32 v9, v9
	v_rcp_f32_e32 v20, v20
	v_rcp_f32_e32 v21, v21
	v_rcp_f32_e32 v22, v22
	v_rcp_f32_e32 v23, v23
	v_pk_mul_f32 v[38:39], v[38:39], v[6:7]
	v_pk_mul_f32 v[40:41], v[40:41], v[8:9]
	v_pk_mul_f32 v[42:43], v[42:43], v[20:21]
	v_pk_mul_f32 v[44:45], v[44:45], v[22:23]
	v_med3_f32 v38, v38, s35, v225
	v_med3_f32 v39, v39, s35, v225
	v_med3_f32 v40, v40, s35, v225
	v_med3_f32 v41, v41, s35, v225
	v_med3_f32 v42, v42, s35, v225
	v_med3_f32 v43, v43, s35, v225
	v_med3_f32 v44, v44, s35, v225
	v_med3_f32 v45, v45, s35, v225
	v_pk_mul_f32 v[46:47], v[46:47], s[34:35] op_sel_hi:[1,0]
	v_pk_mul_f32 v[48:49], v[48:49], s[34:35] op_sel_hi:[1,0]
	v_pk_mul_f32 v[50:51], v[50:51], s[34:35] op_sel_hi:[1,0]
	v_pk_mul_f32 v[52:53], v[52:53], s[34:35] op_sel_hi:[1,0]
	v_pk_mul_f32 v[6:7], v[46:47], s[4:5] op_sel_hi:[1,0]
	v_pk_mul_f32 v[8:9], v[48:49], s[4:5] op_sel_hi:[1,0]
	v_pk_mul_f32 v[20:21], v[50:51], s[4:5] op_sel_hi:[1,0]
	v_pk_mul_f32 v[22:23], v[52:53], s[4:5] op_sel_hi:[1,0]
	v_exp_f32_e32 v6, v6
	v_exp_f32_e32 v7, v7
	v_exp_f32_e32 v8, v8
	v_exp_f32_e32 v9, v9
	v_exp_f32_e32 v20, v20
	v_exp_f32_e32 v21, v21
	v_exp_f32_e32 v22, v22
	v_exp_f32_e32 v23, v23
	v_pk_add_f32 v[6:7], v[6:7], 1.0 op_sel_hi:[1,0]
	v_pk_add_f32 v[8:9], v[8:9], 1.0 op_sel_hi:[1,0]
	v_pk_add_f32 v[20:21], v[20:21], 1.0 op_sel_hi:[1,0]
	v_pk_add_f32 v[22:23], v[22:23], 1.0 op_sel_hi:[1,0]
	v_rcp_f32_e32 v6, v6
	v_rcp_f32_e32 v7, v7
	v_rcp_f32_e32 v8, v8
	v_rcp_f32_e32 v9, v9
	v_rcp_f32_e32 v20, v20
	v_rcp_f32_e32 v21, v21
	v_rcp_f32_e32 v22, v22
	v_rcp_f32_e32 v23, v23
	v_pk_mul_f32 v[46:47], v[46:47], v[6:7]
	v_pk_mul_f32 v[48:49], v[48:49], v[8:9]
	v_pk_mul_f32 v[50:51], v[50:51], v[20:21]
	v_pk_mul_f32 v[52:53], v[52:53], v[22:23]
	v_med3_f32 v46, v46, s35, v225
	v_med3_f32 v47, v47, s35, v225
	v_med3_f32 v48, v48, s35, v225
	v_med3_f32 v49, v49, s35, v225
	v_med3_f32 v50, v50, s35, v225
	v_med3_f32 v51, v51, s35, v225
	v_med3_f32 v52, v52, s35, v225
	v_med3_f32 v53, v53, s35, v225
	v_cvt_pk_fp8_f32 v46, v46, v47
	v_cvt_pk_fp8_f32 v47, v38, v39
	v_cvt_pk_fp8_f32 v46, v48, v49 op_sel:[0,0,1]
	v_cvt_pk_fp8_f32 v47, v40, v41 op_sel:[0,0,1]
	v_cvt_pk_fp8_f32 v48, v50, v51
	v_cvt_pk_fp8_f32 v49, v42, v43
	v_cvt_pk_fp8_f32 v48, v52, v53 op_sel:[0,0,1]
	v_cvt_pk_fp8_f32 v49, v44, v45 op_sel:[0,0,1]
	v_add_co_u32_e32 v14, vcc, 0x2c000, v12
	s_nop 0
	v_permlane16_swap_b32_e32 v46, v48
	v_addc_co_u32_e32 v15, vcc, 0, v13, vcc
	v_permlane16_swap_b32_e32 v47, v49
	global_store_dwordx4 v[14:15], v[46:49], off
